# speedup vs baseline: 1.0409x; 1.0166x over previous
.LBB1_11:
	v_exp_f32_e32 v3, v18
	v_exp_f32_e32 v4, v19
	v_exp_f32_e32 v5, v20
	v_exp_f32_e32 v6, v21
	v_exp_f32_e32 v7, v22
	v_exp_f32_e32 v8, v23
	v_exp_f32_e32 v9, v24
	v_exp_f32_e32 v10, v25
	s_waitcnt vmcnt(20)
	v_cmp_lt_f32_e64 s[38:39], s37, v203
	v_cmp_lt_f32_e64 s[42:43], s37, v205
	v_cmp_lt_f32_e64 s[48:49], s37, v207
	v_cmp_lt_f32_e64 s[50:51], s37, v210
	v_addc_co_u32_e64 v2, s[54:55], v2, v2, s[38:39]
	v_cndmask_b32_e64 v3, v3, 0, s[38:39]
	v_addc_co_u32_e64 v2, s[54:55], v2, v2, s[42:43]
	v_cndmask_b32_e64 v4, v4, 0, s[42:43]
	v_addc_co_u32_e64 v2, s[54:55], v2, v2, s[48:49]
	v_cndmask_b32_e64 v5, v5, 0, s[48:49]
	v_addc_co_u32_e64 v2, s[54:55], v2, v2, s[50:51]
	v_cndmask_b32_e64 v6, v6, 0, s[50:51]
	v_add_f32 v179, v179, v3
	v_add_f32 v178, v178, v4
	v_add_f32 v177, v177, v5
	v_add_f32 v176, v176, v6

	s_lshl_b32 s34, s36, 8
	v_readlane_b32 s36, v240, 14
	v_exp_f32_e32 v11, v26
	v_exp_f32_e32 v12, v27
	v_exp_f32_e32 v13, v28
	v_exp_f32_e32 v14, v29
	s_waitcnt vmcnt(16)
	v_cmp_lt_f32_e64 s[38:39], s37, v204
	v_cmp_lt_f32_e64 s[42:43], s37, v206
	v_cmp_lt_f32_e64 s[48:49], s37, v208
	v_cmp_lt_f32_e64 s[50:51], s37, v211
	v_addc_co_u32_e64 v2, s[54:55], v2, v2, s[38:39]
	v_cndmask_b32_e64 v7, v7, 0, s[38:39]
	v_addc_co_u32_e64 v2, s[54:55], v2, v2, s[42:43]
	v_cndmask_b32_e64 v8, v8, 0, s[42:43]
	v_addc_co_u32_e64 v2, s[54:55], v2, v2, s[48:49]
	v_cndmask_b32_e64 v9, v9, 0, s[48:49]
	v_addc_co_u32_e64 v2, s[54:55], v2, v2, s[50:51]
	v_cndmask_b32_e64 v10, v10, 0, s[50:51]
	v_add_f32 v175, v175, v7
	v_add_f32 v174, v174, v8
	v_add_f32 v173, v173, v9
	v_add_f32 v172, v172, v10

	s_add_i32 s34, s36, s34
	v_exp_f32_e32 v15, v30
	v_exp_f32_e32 v16, v31
	v_exp_f32_e32 v17, v32
	v_exp_f32_e32 v18, v33
	s_waitcnt vmcnt(12)
	v_cmp_lt_f32_e64 s[38:39], s37, v212
	v_cmp_lt_f32_e64 s[42:43], s37, v213
	v_cmp_lt_f32_e64 s[48:49], s37, v214
	v_cmp_lt_f32_e64 s[50:51], s37, v215
	v_addc_co_u32_e64 v2, s[54:55], v2, v2, s[38:39]
	v_cndmask_b32_e64 v11, v11, 0, s[38:39]
	v_addc_co_u32_e64 v2, s[54:55], v2, v2, s[42:43]
	v_cndmask_b32_e64 v12, v12, 0, s[42:43]
	v_addc_co_u32_e64 v2, s[54:55], v2, v2, s[48:49]
	v_cndmask_b32_e64 v13, v13, 0, s[48:49]
	v_addc_co_u32_e64 v2, s[54:55], v2, v2, s[50:51]
	v_cndmask_b32_e64 v14, v14, 0, s[50:51]
	v_add_f32 v171, v171, v11
	v_add_f32 v170, v170, v12
	v_add_f32 v169, v169, v13
	v_add_f32 v168, v168, v14

	v_lshl_add_u32 v3, v194, 2, s34
	s_waitcnt vmcnt(8)
	v_cmp_lt_f32_e64 s[38:39], s37, v190
	v_cmp_lt_f32_e64 s[42:43], s37, v192
	v_cmp_lt_f32_e64 s[48:49], s37, v193
	v_cmp_lt_f32_e64 s[50:51], s37, v202
	v_addc_co_u32_e64 v2, s[54:55], v2, v2, s[38:39]
	v_cndmask_b32_e64 v15, v15, 0, s[38:39]
	v_addc_co_u32_e64 v2, s[54:55], v2, v2, s[42:43]
	v_cndmask_b32_e64 v16, v16, 0, s[42:43]
	v_addc_co_u32_e64 v2, s[54:55], v2, v2, s[48:49]
	v_cndmask_b32_e64 v17, v17, 0, s[48:49]
	v_addc_co_u32_e64 v2, s[54:55], v2, v2, s[50:51]
	v_cndmask_b32_e64 v18, v18, 0, s[50:51]
	v_add_f32 v167, v167, v15
	v_add_f32 v166, v166, v16
	v_add_f32 v165, v165, v17
	v_add_f32 v164, v164, v18

	ds_write_b32 v3, v2
	s_lshl_b32 s38, s52, 8
	s_add_i32 s34, s38, 0x8800
	s_add_i32 s38, s38, 0x8000
	v_cmp_eq_u32_e32 vcc, 16, v163
	v_lshl_add_u32 v3, v160, 2, s34
	v_lshl_add_u32 v152, v160, 2, s38
	v_add_f32_dpp v227, v227, v227 quad_perm:[1,0,3,2] row_mask:0xf bank_mask:0xf bound_ctrl:1
	v_add_f32_dpp v224, v224, v224 quad_perm:[1,0,3,2] row_mask:0xf bank_mask:0xf bound_ctrl:1
	v_add_f32_dpp v217, v217, v217 quad_perm:[1,0,3,2] row_mask:0xf bank_mask:0xf bound_ctrl:1
	v_add_f32_dpp v216, v216, v216 quad_perm:[1,0,3,2] row_mask:0xf bank_mask:0xf bound_ctrl:1
	v_add_f32_dpp v209, v209, v209 quad_perm:[1,0,3,2] row_mask:0xf bank_mask:0xf bound_ctrl:1
	v_add_f32_dpp v191, v191, v191 quad_perm:[1,0,3,2] row_mask:0xf bank_mask:0xf bound_ctrl:1
	v_add_f32_dpp v189, v189, v189 quad_perm:[1,0,3,2] row_mask:0xf bank_mask:0xf bound_ctrl:1
	v_add_f32_dpp v188, v188, v188 quad_perm:[1,0,3,2] row_mask:0xf bank_mask:0xf bound_ctrl:1
	v_add_f32_dpp v187, v187, v187 quad_perm:[1,0,3,2] row_mask:0xf bank_mask:0xf bound_ctrl:1
	v_add_f32_dpp v186, v186, v186 quad_perm:[1,0,3,2] row_mask:0xf bank_mask:0xf bound_ctrl:1
	v_add_f32_dpp v185, v185, v185 quad_perm:[1,0,3,2] row_mask:0xf bank_mask:0xf bound_ctrl:1
	v_add_f32_dpp v184, v184, v184 quad_perm:[1,0,3,2] row_mask:0xf bank_mask:0xf bound_ctrl:1
	v_add_f32_dpp v183, v183, v183 quad_perm:[1,0,3,2] row_mask:0xf bank_mask:0xf bound_ctrl:1
	v_add_f32_dpp v182, v182, v182 quad_perm:[1,0,3,2] row_mask:0xf bank_mask:0xf bound_ctrl:1
	v_add_f32_dpp v181, v181, v181 quad_perm:[1,0,3,2] row_mask:0xf bank_mask:0xf bound_ctrl:1
	v_add_f32_dpp v180, v180, v180 quad_perm:[1,0,3,2] row_mask:0xf bank_mask:0xf bound_ctrl:1
	v_add_f32_dpp v179, v179, v179 quad_perm:[1,0,3,2] row_mask:0xf bank_mask:0xf bound_ctrl:1
	v_add_f32_dpp v178, v178, v178 quad_perm:[1,0,3,2] row_mask:0xf bank_mask:0xf bound_ctrl:1
	v_add_f32_dpp v177, v177, v177 quad_perm:[1,0,3,2] row_mask:0xf bank_mask:0xf bound_ctrl:1
	v_add_f32_dpp v176, v176, v176 quad_perm:[1,0,3,2] row_mask:0xf bank_mask:0xf bound_ctrl:1
	v_add_f32_dpp v175, v175, v175 quad_perm:[1,0,3,2] row_mask:0xf bank_mask:0xf bound_ctrl:1
	v_add_f32_dpp v174, v174, v174 quad_perm:[1,0,3,2] row_mask:0xf bank_mask:0xf bound_ctrl:1
	v_add_f32_dpp v173, v173, v173 quad_perm:[1,0,3,2] row_mask:0xf bank_mask:0xf bound_ctrl:1
	v_add_f32_dpp v172, v172, v172 quad_perm:[1,0,3,2] row_mask:0xf bank_mask:0xf bound_ctrl:1
	v_add_f32_dpp v171, v171, v171 quad_perm:[1,0,3,2] row_mask:0xf bank_mask:0xf bound_ctrl:1
	v_add_f32_dpp v170, v170, v170 quad_perm:[1,0,3,2] row_mask:0xf bank_mask:0xf bound_ctrl:1
	v_add_f32_dpp v169, v169, v169 quad_perm:[1,0,3,2] row_mask:0xf bank_mask:0xf bound_ctrl:1
	v_add_f32_dpp v168, v168, v168 quad_perm:[1,0,3,2] row_mask:0xf bank_mask:0xf bound_ctrl:1
	v_add_f32_dpp v167, v167, v167 quad_perm:[1,0,3,2] row_mask:0xf bank_mask:0xf bound_ctrl:1
	v_add_f32_dpp v166, v166, v166 quad_perm:[1,0,3,2] row_mask:0xf bank_mask:0xf bound_ctrl:1
	v_add_f32_dpp v165, v165, v165 quad_perm:[1,0,3,2] row_mask:0xf bank_mask:0xf bound_ctrl:1
	v_add_f32_dpp v164, v164, v164 quad_perm:[1,0,3,2] row_mask:0xf bank_mask:0xf bound_ctrl:1
	v_add_f32_dpp v227, v227, v227 quad_perm:[2,3,0,1] row_mask:0xf bank_mask:0xf bound_ctrl:1
	v_add_f32_dpp v224, v224, v224 quad_perm:[2,3,0,1] row_mask:0xf bank_mask:0xf bound_ctrl:1
	v_add_f32_dpp v217, v217, v217 quad_perm:[2,3,0,1] row_mask:0xf bank_mask:0xf bound_ctrl:1
	v_add_f32_dpp v216, v216, v216 quad_perm:[2,3,0,1] row_mask:0xf bank_mask:0xf bound_ctrl:1
	v_add_f32_dpp v209, v209, v209 quad_perm:[2,3,0,1] row_mask:0xf bank_mask:0xf bound_ctrl:1
	v_add_f32_dpp v191, v191, v191 quad_perm:[2,3,0,1] row_mask:0xf bank_mask:0xf bound_ctrl:1
	v_add_f32_dpp v189, v189, v189 quad_perm:[2,3,0,1] row_mask:0xf bank_mask:0xf bound_ctrl:1
	v_add_f32_dpp v188, v188, v188 quad_perm:[2,3,0,1] row_mask:0xf bank_mask:0xf bound_ctrl:1
	v_add_f32_dpp v187, v187, v187 quad_perm:[2,3,0,1] row_mask:0xf bank_mask:0xf bound_ctrl:1
	v_add_f32_dpp v186, v186, v186 quad_perm:[2,3,0,1] row_mask:0xf bank_mask:0xf bound_ctrl:1
	v_add_f32_dpp v185, v185, v185 quad_perm:[2,3,0,1] row_mask:0xf bank_mask:0xf bound_ctrl:1
	v_add_f32_dpp v184, v184, v184 quad_perm:[2,3,0,1] row_mask:0xf bank_mask:0xf bound_ctrl:1
	v_add_f32_dpp v183, v183, v183 quad_perm:[2,3,0,1] row_mask:0xf bank_mask:0xf bound_ctrl:1
	v_add_f32_dpp v182, v182, v182 quad_perm:[2,3,0,1] row_mask:0xf bank_mask:0xf bound_ctrl:1
	v_add_f32_dpp v181, v181, v181 quad_perm:[2,3,0,1] row_mask:0xf bank_mask:0xf bound_ctrl:1
	v_add_f32_dpp v180, v180, v180 quad_perm:[2,3,0,1] row_mask:0xf bank_mask:0xf bound_ctrl:1
	v_add_f32_dpp v179, v179, v179 quad_perm:[2,3,0,1] row_mask:0xf bank_mask:0xf bound_ctrl:1
	v_add_f32_dpp v178, v178, v178 quad_perm:[2,3,0,1] row_mask:0xf bank_mask:0xf bound_ctrl:1
	v_add_f32_dpp v177, v177, v177 quad_perm:[2,3,0,1] row_mask:0xf bank_mask:0xf bound_ctrl:1
	v_add_f32_dpp v176, v176, v176 quad_perm:[2,3,0,1] row_mask:0xf bank_mask:0xf bound_ctrl:1
	v_add_f32_dpp v175, v175, v175 quad_perm:[2,3,0,1] row_mask:0xf bank_mask:0xf bound_ctrl:1
	v_add_f32_dpp v174, v174, v174 quad_perm:[2,3,0,1] row_mask:0xf bank_mask:0xf bound_ctrl:1
	v_add_f32_dpp v173, v173, v173 quad_perm:[2,3,0,1] row_mask:0xf bank_mask:0xf bound_ctrl:1
	v_add_f32_dpp v172, v172, v172 quad_perm:[2,3,0,1] row_mask:0xf bank_mask:0xf bound_ctrl:1
	v_add_f32_dpp v171, v171, v171 quad_perm:[2,3,0,1] row_mask:0xf bank_mask:0xf bound_ctrl:1
	v_add_f32_dpp v170, v170, v170 quad_perm:[2,3,0,1] row_mask:0xf bank_mask:0xf bound_ctrl:1
	v_add_f32_dpp v169, v169, v169 quad_perm:[2,3,0,1] row_mask:0xf bank_mask:0xf bound_ctrl:1
	v_add_f32_dpp v168, v168, v168 quad_perm:[2,3,0,1] row_mask:0xf bank_mask:0xf bound_ctrl:1
	v_add_f32_dpp v167, v167, v167 quad_perm:[2,3,0,1] row_mask:0xf bank_mask:0xf bound_ctrl:1
	v_add_f32_dpp v166, v166, v166 quad_perm:[2,3,0,1] row_mask:0xf bank_mask:0xf bound_ctrl:1
	v_add_f32_dpp v165, v165, v165 quad_perm:[2,3,0,1] row_mask:0xf bank_mask:0xf bound_ctrl:1
	v_add_f32_dpp v164, v164, v164 quad_perm:[2,3,0,1] row_mask:0xf bank_mask:0xf bound_ctrl:1
	v_add_f32_dpp v227, v227, v227 row_half_mirror row_mask:0xf bank_mask:0xf bound_ctrl:1
	v_add_f32_dpp v224, v224, v224 row_half_mirror row_mask:0xf bank_mask:0xf bound_ctrl:1
	v_add_f32_dpp v217, v217, v217 row_half_mirror row_mask:0xf bank_mask:0xf bound_ctrl:1
	v_add_f32_dpp v216, v216, v216 row_half_mirror row_mask:0xf bank_mask:0xf bound_ctrl:1
	v_add_f32_dpp v209, v209, v209 row_half_mirror row_mask:0xf bank_mask:0xf bound_ctrl:1
	v_add_f32_dpp v191, v191, v191 row_half_mirror row_mask:0xf bank_mask:0xf bound_ctrl:1
	v_add_f32_dpp v189, v189, v189 row_half_mirror row_mask:0xf bank_mask:0xf bound_ctrl:1
	v_add_f32_dpp v188, v188, v188 row_half_mirror row_mask:0xf bank_mask:0xf bound_ctrl:1
	v_add_f32_dpp v187, v187, v187 row_half_mirror row_mask:0xf bank_mask:0xf bound_ctrl:1
	v_add_f32_dpp v186, v186, v186 row_half_mirror row_mask:0xf bank_mask:0xf bound_ctrl:1
	v_add_f32_dpp v185, v185, v185 row_half_mirror row_mask:0xf bank_mask:0xf bound_ctrl:1
	v_add_f32_dpp v184, v184, v184 row_half_mirror row_mask:0xf bank_mask:0xf bound_ctrl:1
	v_add_f32_dpp v183, v183, v183 row_half_mirror row_mask:0xf bank_mask:0xf bound_ctrl:1
	v_add_f32_dpp v182, v182, v182 row_half_mirror row_mask:0xf bank_mask:0xf bound_ctrl:1
	v_add_f32_dpp v181, v181, v181 row_half_mirror row_mask:0xf bank_mask:0xf bound_ctrl:1
	v_add_f32_dpp v180, v180, v180 row_half_mirror row_mask:0xf bank_mask:0xf bound_ctrl:1
	v_add_f32_dpp v179, v179, v179 row_half_mirror row_mask:0xf bank_mask:0xf bound_ctrl:1
	v_add_f32_dpp v178, v178, v178 row_half_mirror row_mask:0xf bank_mask:0xf bound_ctrl:1
	v_add_f32_dpp v177, v177, v177 row_half_mirror row_mask:0xf bank_mask:0xf bound_ctrl:1
	v_add_f32_dpp v176, v176, v176 row_half_mirror row_mask:0xf bank_mask:0xf bound_ctrl:1
	v_add_f32_dpp v175, v175, v175 row_half_mirror row_mask:0xf bank_mask:0xf bound_ctrl:1
	v_add_f32_dpp v174, v174, v174 row_half_mirror row_mask:0xf bank_mask:0xf bound_ctrl:1
	v_add_f32_dpp v173, v173, v173 row_half_mirror row_mask:0xf bank_mask:0xf bound_ctrl:1
	v_add_f32_dpp v172, v172, v172 row_half_mirror row_mask:0xf bank_mask:0xf bound_ctrl:1
	v_add_f32_dpp v171, v171, v171 row_half_mirror row_mask:0xf bank_mask:0xf bound_ctrl:1
	v_add_f32_dpp v170, v170, v170 row_half_mirror row_mask:0xf bank_mask:0xf bound_ctrl:1
	v_add_f32_dpp v169, v169, v169 row_half_mirror row_mask:0xf bank_mask:0xf bound_ctrl:1
	v_add_f32_dpp v168, v168, v168 row_half_mirror row_mask:0xf bank_mask:0xf bound_ctrl:1
	v_add_f32_dpp v167, v167, v167 row_half_mirror row_mask:0xf bank_mask:0xf bound_ctrl:1
	v_add_f32_dpp v166, v166, v166 row_half_mirror row_mask:0xf bank_mask:0xf bound_ctrl:1
	v_add_f32_dpp v165, v165, v165 row_half_mirror row_mask:0xf bank_mask:0xf bound_ctrl:1
	v_add_f32_dpp v164, v164, v164 row_half_mirror row_mask:0xf bank_mask:0xf bound_ctrl:1
	v_add_f32_dpp v227, v227, v227 row_mirror row_mask:0xf bank_mask:0xf bound_ctrl:1
	v_add_f32_dpp v224, v224, v224 row_mirror row_mask:0xf bank_mask:0xf bound_ctrl:1
	v_add_f32_dpp v217, v217, v217 row_mirror row_mask:0xf bank_mask:0xf bound_ctrl:1
	v_add_f32_dpp v216, v216, v216 row_mirror row_mask:0xf bank_mask:0xf bound_ctrl:1
	v_add_f32_dpp v209, v209, v209 row_mirror row_mask:0xf bank_mask:0xf bound_ctrl:1
	v_add_f32_dpp v191, v191, v191 row_mirror row_mask:0xf bank_mask:0xf bound_ctrl:1
	v_add_f32_dpp v189, v189, v189 row_mirror row_mask:0xf bank_mask:0xf bound_ctrl:1
	v_add_f32_dpp v188, v188, v188 row_mirror row_mask:0xf bank_mask:0xf bound_ctrl:1
	v_add_f32_dpp v187, v187, v187 row_mirror row_mask:0xf bank_mask:0xf bound_ctrl:1
	v_add_f32_dpp v186, v186, v186 row_mirror row_mask:0xf bank_mask:0xf bound_ctrl:1
	v_add_f32_dpp v185, v185, v185 row_mirror row_mask:0xf bank_mask:0xf bound_ctrl:1
	v_add_f32_dpp v184, v184, v184 row_mirror row_mask:0xf bank_mask:0xf bound_ctrl:1
	v_add_f32_dpp v183, v183, v183 row_mirror row_mask:0xf bank_mask:0xf bound_ctrl:1
	v_add_f32_dpp v182, v182, v182 row_mirror row_mask:0xf bank_mask:0xf bound_ctrl:1
	v_add_f32_dpp v181, v181, v181 row_mirror row_mask:0xf bank_mask:0xf bound_ctrl:1
	v_add_f32_dpp v180, v180, v180 row_mirror row_mask:0xf bank_mask:0xf bound_ctrl:1
	v_add_f32_dpp v179, v179, v179 row_mirror row_mask:0xf bank_mask:0xf bound_ctrl:1
	v_add_f32_dpp v178, v178, v178 row_mirror row_mask:0xf bank_mask:0xf bound_ctrl:1
	v_add_f32_dpp v177, v177, v177 row_mirror row_mask:0xf bank_mask:0xf bound_ctrl:1
	v_add_f32_dpp v176, v176, v176 row_mirror row_mask:0xf bank_mask:0xf bound_ctrl:1
	v_add_f32_dpp v175, v175, v175 row_mirror row_mask:0xf bank_mask:0xf bound_ctrl:1
	v_add_f32_dpp v174, v174, v174 row_mirror row_mask:0xf bank_mask:0xf bound_ctrl:1
	v_add_f32_dpp v173, v173, v173 row_mirror row_mask:0xf bank_mask:0xf bound_ctrl:1
	v_add_f32_dpp v172, v172, v172 row_mirror row_mask:0xf bank_mask:0xf bound_ctrl:1
	v_add_f32_dpp v171, v171, v171 row_mirror row_mask:0xf bank_mask:0xf bound_ctrl:1
	v_add_f32_dpp v170, v170, v170 row_mirror row_mask:0xf bank_mask:0xf bound_ctrl:1
	v_add_f32_dpp v169, v169, v169 row_mirror row_mask:0xf bank_mask:0xf bound_ctrl:1
	v_add_f32_dpp v168, v168, v168 row_mirror row_mask:0xf bank_mask:0xf bound_ctrl:1
	v_add_f32_dpp v167, v167, v167 row_mirror row_mask:0xf bank_mask:0xf bound_ctrl:1
	v_add_f32_dpp v166, v166, v166 row_mirror row_mask:0xf bank_mask:0xf bound_ctrl:1
	v_add_f32_dpp v165, v165, v165 row_mirror row_mask:0xf bank_mask:0xf bound_ctrl:1
	v_add_f32_dpp v164, v164, v164 row_mirror row_mask:0xf bank_mask:0xf bound_ctrl:1
	v_mov_b32_dpp v4, v227 row_bcast:15 row_mask:0xa bank_mask:0xf bound_ctrl:1
	v_mov_b32_dpp v5, v224 row_bcast:15 row_mask:0xa bank_mask:0xf bound_ctrl:1
	v_mov_b32_dpp v6, v217 row_bcast:15 row_mask:0xa bank_mask:0xf bound_ctrl:1
	v_mov_b32_dpp v7, v216 row_bcast:15 row_mask:0xa bank_mask:0xf bound_ctrl:1
	v_mov_b32_dpp v8, v209 row_bcast:15 row_mask:0xa bank_mask:0xf bound_ctrl:1
	v_mov_b32_dpp v9, v191 row_bcast:15 row_mask:0xa bank_mask:0xf bound_ctrl:1
	v_mov_b32_dpp v10, v189 row_bcast:15 row_mask:0xa bank_mask:0xf bound_ctrl:1
	v_mov_b32_dpp v11, v188 row_bcast:15 row_mask:0xa bank_mask:0xf bound_ctrl:1
	v_mov_b32_dpp v12, v187 row_bcast:15 row_mask:0xa bank_mask:0xf bound_ctrl:1
	v_mov_b32_dpp v13, v186 row_bcast:15 row_mask:0xa bank_mask:0xf bound_ctrl:1
	v_mov_b32_dpp v14, v185 row_bcast:15 row_mask:0xa bank_mask:0xf bound_ctrl:1
	v_mov_b32_dpp v15, v184 row_bcast:15 row_mask:0xa bank_mask:0xf bound_ctrl:1
	v_mov_b32_dpp v16, v183 row_bcast:15 row_mask:0xa bank_mask:0xf bound_ctrl:1
	v_mov_b32_dpp v17, v182 row_bcast:15 row_mask:0xa bank_mask:0xf bound_ctrl:1
	v_mov_b32_dpp v18, v181 row_bcast:15 row_mask:0xa bank_mask:0xf bound_ctrl:1
	v_mov_b32_dpp v19, v180 row_bcast:15 row_mask:0xa bank_mask:0xf bound_ctrl:1
	v_mov_b32_dpp v20, v179 row_bcast:15 row_mask:0xa bank_mask:0xf bound_ctrl:1
	v_mov_b32_dpp v21, v178 row_bcast:15 row_mask:0xa bank_mask:0xf bound_ctrl:1
	v_mov_b32_dpp v22, v177 row_bcast:15 row_mask:0xa bank_mask:0xf bound_ctrl:1
	v_mov_b32_dpp v23, v176 row_bcast:15 row_mask:0xa bank_mask:0xf bound_ctrl:1
	v_mov_b32_dpp v24, v175 row_bcast:15 row_mask:0xa bank_mask:0xf bound_ctrl:1
	v_mov_b32_dpp v25, v174 row_bcast:15 row_mask:0xa bank_mask:0xf bound_ctrl:1
	v_mov_b32_dpp v26, v173 row_bcast:15 row_mask:0xa bank_mask:0xf bound_ctrl:1
	v_mov_b32_dpp v27, v172 row_bcast:15 row_mask:0xa bank_mask:0xf bound_ctrl:1
	v_mov_b32_dpp v28, v171 row_bcast:15 row_mask:0xa bank_mask:0xf bound_ctrl:1
	v_mov_b32_dpp v29, v170 row_bcast:15 row_mask:0xa bank_mask:0xf bound_ctrl:1
	v_mov_b32_dpp v30, v169 row_bcast:15 row_mask:0xa bank_mask:0xf bound_ctrl:1
	v_mov_b32_dpp v31, v168 row_bcast:15 row_mask:0xa bank_mask:0xf bound_ctrl:1
	v_mov_b32_dpp v32, v167 row_bcast:15 row_mask:0xa bank_mask:0xf bound_ctrl:1
	v_mov_b32_dpp v33, v166 row_bcast:15 row_mask:0xa bank_mask:0xf bound_ctrl:1
	v_mov_b32_dpp v130, v165 row_bcast:15 row_mask:0xa bank_mask:0xf bound_ctrl:1
	v_mov_b32_dpp v131, v164 row_bcast:15 row_mask:0xa bank_mask:0xf bound_ctrl:1
	s_and_saveexec_b64 s[36:37], vcc
	v_add_f32_e32 v227, v227, v4
	v_add_f32_e32 v224, v224, v5
	v_add_f32_e32 v217, v217, v6
	v_add_f32_e32 v216, v216, v7
	v_add_f32_e32 v209, v209, v8
	v_add_f32_e32 v191, v191, v9
	v_add_f32_e32 v189, v189, v10
	v_add_f32_e32 v188, v188, v11
	v_add_f32_e32 v187, v187, v12
	v_add_f32_e32 v186, v186, v13
	v_add_f32_e32 v185, v185, v14
	v_add_f32_e32 v184, v184, v15
	v_add_f32_e32 v183, v183, v16
	v_add_f32_e32 v182, v182, v17
	v_add_f32_e32 v181, v181, v18
	v_add_f32_e32 v180, v180, v19
	v_add_f32_e32 v179, v179, v20
	v_add_f32_e32 v178, v178, v21
	v_add_f32_e32 v177, v177, v22
	v_add_f32_e32 v176, v176, v23
	v_add_f32_e32 v175, v175, v24
	v_add_f32_e32 v174, v174, v25
	v_add_f32_e32 v173, v173, v26
	v_add_f32_e32 v172, v172, v27
	v_add_f32_e32 v171, v171, v28
	v_add_f32_e32 v170, v170, v29
	v_add_f32_e32 v169, v169, v30
	v_add_f32_e32 v168, v168, v31
	v_add_f32_e32 v167, v167, v32
	v_add_f32_e32 v166, v166, v33
	v_add_f32_e32 v165, v165, v130
	v_add_f32_e32 v164, v164, v131
	ds_write_b32 v3, v227
	ds_write_b32 v3, v224 offset:4
	ds_write_b32 v3, v217 offset:8
	ds_write_b32 v3, v216 offset:12
	ds_write_b32 v3, v209 offset:32
	ds_write_b32 v3, v191 offset:36
	ds_write_b32 v3, v189 offset:40
	ds_write_b32 v3, v188 offset:44
	ds_write_b32 v3, v187 offset:64
	ds_write_b32 v3, v186 offset:68
	ds_write_b32 v3, v185 offset:72
	ds_write_b32 v3, v184 offset:76
	ds_write_b32 v3, v183 offset:96
	ds_write_b32 v3, v182 offset:100
	ds_write_b32 v3, v181 offset:104
	ds_write_b32 v3, v180 offset:108
	ds_write_b32 v3, v179 offset:128
	ds_write_b32 v3, v178 offset:132
	ds_write_b32 v3, v177 offset:136
	ds_write_b32 v3, v176 offset:140
	ds_write_b32 v3, v175 offset:160
	ds_write_b32 v3, v174 offset:164
	ds_write_b32 v3, v173 offset:168
	ds_write_b32 v3, v172 offset:172
	ds_write_b32 v3, v171 offset:192
	ds_write_b32 v3, v170 offset:196
	ds_write_b32 v3, v169 offset:200
	ds_write_b32 v3, v168 offset:204
	ds_write_b32 v3, v167 offset:224
	ds_write_b32 v3, v166 offset:228
	ds_write_b32 v3, v165 offset:232
	ds_write_b32 v3, v164 offset:236
	s_or_b64 exec, exec, s[36:37]
	v_lshrrev_b32_e32 v4, 4, v2
	v_and_b32_e32 v5, 0x1010101, v2
	v_and_b32_e32 v6, 0x1010101, v4
	v_add_u32_e32 v162, v162, v5
	v_add_u32_e32 v157, v157, v6
	v_and_b32_e32 v5, 0x2020202, v2
	v_and_b32_e32 v6, 0x2020202, v4
	v_add_u32_e32 v161, v161, v5
	v_add_u32_e32 v156, v156, v6
	v_and_b32_e32 v5, 0x4040404, v2
	v_and_b32_e32 v6, 0x4040404, v4
	v_add_u32_e32 v159, v159, v5
	v_add_u32_e32 v155, v155, v6
	v_and_b32_e32 v5, 0x8080808, v2
	v_and_b32_e32 v6, 0x8080808, v4
	v_add_u32_e32 v158, v158, v5
	v_add_u32_e32 v154, v154, v6
	v_lshrrev_b32_e32 v161, 1, v161
	v_lshrrev_b32_e32 v159, 2, v159
	v_lshrrev_b32_e32 v158, 3, v158
	v_lshrrev_b32_e32 v156, 1, v156
	v_lshrrev_b32_e32 v155, 2, v155
	v_lshrrev_b32_e32 v154, 3, v154
	v_and_b32_e32 v8, 0xff00ff, v162
	v_lshrrev_b32_e32 v16, 8, v162
	v_and_b32_e32 v9, 0xff00ff, v161
	v_lshrrev_b32_e32 v17, 8, v161
	v_and_b32_e32 v10, 0xff00ff, v159
	v_lshrrev_b32_e32 v18, 8, v159
	v_and_b32_e32 v11, 0xff00ff, v158
	v_lshrrev_b32_e32 v19, 8, v158
	v_and_b32_e32 v12, 0xff00ff, v157
	v_lshrrev_b32_e32 v20, 8, v157
	v_and_b32_e32 v13, 0xff00ff, v156
	v_lshrrev_b32_e32 v21, 8, v156
	v_and_b32_e32 v14, 0xff00ff, v155
	v_lshrrev_b32_e32 v22, 8, v155
	v_and_b32_e32 v15, 0xff00ff, v154
	v_lshrrev_b32_e32 v23, 8, v154
	v_and_b32_e32 v16, 0xff00ff, v16
	v_and_b32_e32 v17, 0xff00ff, v17
	v_and_b32_e32 v18, 0xff00ff, v18
	v_and_b32_e32 v19, 0xff00ff, v19
	v_and_b32_e32 v20, 0xff00ff, v20
	v_and_b32_e32 v21, 0xff00ff, v21
	v_and_b32_e32 v22, 0xff00ff, v22
	v_and_b32_e32 v23, 0xff00ff, v23
	v_add_u32_dpp v8, v8, v8 quad_perm:[1,0,3,2] row_mask:0xf bank_mask:0xf bound_ctrl:1
	v_add_u32_dpp v9, v9, v9 quad_perm:[1,0,3,2] row_mask:0xf bank_mask:0xf bound_ctrl:1
	v_add_u32_dpp v10, v10, v10 quad_perm:[1,0,3,2] row_mask:0xf bank_mask:0xf bound_ctrl:1
	v_add_u32_dpp v11, v11, v11 quad_perm:[1,0,3,2] row_mask:0xf bank_mask:0xf bound_ctrl:1
	v_add_u32_dpp v12, v12, v12 quad_perm:[1,0,3,2] row_mask:0xf bank_mask:0xf bound_ctrl:1
	v_add_u32_dpp v13, v13, v13 quad_perm:[1,0,3,2] row_mask:0xf bank_mask:0xf bound_ctrl:1
	v_add_u32_dpp v14, v14, v14 quad_perm:[1,0,3,2] row_mask:0xf bank_mask:0xf bound_ctrl:1
	v_add_u32_dpp v15, v15, v15 quad_perm:[1,0,3,2] row_mask:0xf bank_mask:0xf bound_ctrl:1
	v_add_u32_dpp v16, v16, v16 quad_perm:[1,0,3,2] row_mask:0xf bank_mask:0xf bound_ctrl:1
	v_add_u32_dpp v17, v17, v17 quad_perm:[1,0,3,2] row_mask:0xf bank_mask:0xf bound_ctrl:1
	v_add_u32_dpp v18, v18, v18 quad_perm:[1,0,3,2] row_mask:0xf bank_mask:0xf bound_ctrl:1
	v_add_u32_dpp v19, v19, v19 quad_perm:[1,0,3,2] row_mask:0xf bank_mask:0xf bound_ctrl:1
	v_add_u32_dpp v20, v20, v20 quad_perm:[1,0,3,2] row_mask:0xf bank_mask:0xf bound_ctrl:1
	v_add_u32_dpp v21, v21, v21 quad_perm:[1,0,3,2] row_mask:0xf bank_mask:0xf bound_ctrl:1
	v_add_u32_dpp v22, v22, v22 quad_perm:[1,0,3,2] row_mask:0xf bank_mask:0xf bound_ctrl:1
	v_add_u32_dpp v23, v23, v23 quad_perm:[1,0,3,2] row_mask:0xf bank_mask:0xf bound_ctrl:1
	v_add_u32_dpp v8, v8, v8 quad_perm:[2,3,0,1] row_mask:0xf bank_mask:0xf bound_ctrl:1
	v_add_u32_dpp v9, v9, v9 quad_perm:[2,3,0,1] row_mask:0xf bank_mask:0xf bound_ctrl:1
	v_add_u32_dpp v10, v10, v10 quad_perm:[2,3,0,1] row_mask:0xf bank_mask:0xf bound_ctrl:1
	v_add_u32_dpp v11, v11, v11 quad_perm:[2,3,0,1] row_mask:0xf bank_mask:0xf bound_ctrl:1
	v_add_u32_dpp v12, v12, v12 quad_perm:[2,3,0,1] row_mask:0xf bank_mask:0xf bound_ctrl:1
	v_add_u32_dpp v13, v13, v13 quad_perm:[2,3,0,1] row_mask:0xf bank_mask:0xf bound_ctrl:1
	v_add_u32_dpp v14, v14, v14 quad_perm:[2,3,0,1] row_mask:0xf bank_mask:0xf bound_ctrl:1
	v_add_u32_dpp v15, v15, v15 quad_perm:[2,3,0,1] row_mask:0xf bank_mask:0xf bound_ctrl:1
	v_add_u32_dpp v16, v16, v16 quad_perm:[2,3,0,1] row_mask:0xf bank_mask:0xf bound_ctrl:1
	v_add_u32_dpp v17, v17, v17 quad_perm:[2,3,0,1] row_mask:0xf bank_mask:0xf bound_ctrl:1
	v_add_u32_dpp v18, v18, v18 quad_perm:[2,3,0,1] row_mask:0xf bank_mask:0xf bound_ctrl:1
	v_add_u32_dpp v19, v19, v19 quad_perm:[2,3,0,1] row_mask:0xf bank_mask:0xf bound_ctrl:1
	v_add_u32_dpp v20, v20, v20 quad_perm:[2,3,0,1] row_mask:0xf bank_mask:0xf bound_ctrl:1
	v_add_u32_dpp v21, v21, v21 quad_perm:[2,3,0,1] row_mask:0xf bank_mask:0xf bound_ctrl:1
	v_add_u32_dpp v22, v22, v22 quad_perm:[2,3,0,1] row_mask:0xf bank_mask:0xf bound_ctrl:1
	v_add_u32_dpp v23, v23, v23 quad_perm:[2,3,0,1] row_mask:0xf bank_mask:0xf bound_ctrl:1
	v_add_u32_dpp v8, v8, v8 row_half_mirror row_mask:0xf bank_mask:0xf bound_ctrl:1
	v_add_u32_dpp v9, v9, v9 row_half_mirror row_mask:0xf bank_mask:0xf bound_ctrl:1
	v_add_u32_dpp v10, v10, v10 row_half_mirror row_mask:0xf bank_mask:0xf bound_ctrl:1
	v_add_u32_dpp v11, v11, v11 row_half_mirror row_mask:0xf bank_mask:0xf bound_ctrl:1
	v_add_u32_dpp v12, v12, v12 row_half_mirror row_mask:0xf bank_mask:0xf bound_ctrl:1
	v_add_u32_dpp v13, v13, v13 row_half_mirror row_mask:0xf bank_mask:0xf bound_ctrl:1
	v_add_u32_dpp v14, v14, v14 row_half_mirror row_mask:0xf bank_mask:0xf bound_ctrl:1
	v_add_u32_dpp v15, v15, v15 row_half_mirror row_mask:0xf bank_mask:0xf bound_ctrl:1
	v_add_u32_dpp v16, v16, v16 row_half_mirror row_mask:0xf bank_mask:0xf bound_ctrl:1
	v_add_u32_dpp v17, v17, v17 row_half_mirror row_mask:0xf bank_mask:0xf bound_ctrl:1
	v_add_u32_dpp v18, v18, v18 row_half_mirror row_mask:0xf bank_mask:0xf bound_ctrl:1
	v_add_u32_dpp v19, v19, v19 row_half_mirror row_mask:0xf bank_mask:0xf bound_ctrl:1
	v_add_u32_dpp v20, v20, v20 row_half_mirror row_mask:0xf bank_mask:0xf bound_ctrl:1
	v_add_u32_dpp v21, v21, v21 row_half_mirror row_mask:0xf bank_mask:0xf bound_ctrl:1
	v_add_u32_dpp v22, v22, v22 row_half_mirror row_mask:0xf bank_mask:0xf bound_ctrl:1
	v_add_u32_dpp v23, v23, v23 row_half_mirror row_mask:0xf bank_mask:0xf bound_ctrl:1
	v_add_u32_dpp v8, v8, v8 row_mirror row_mask:0xf bank_mask:0xf bound_ctrl:1
	v_add_u32_dpp v9, v9, v9 row_mirror row_mask:0xf bank_mask:0xf bound_ctrl:1
	v_add_u32_dpp v10, v10, v10 row_mirror row_mask:0xf bank_mask:0xf bound_ctrl:1
	v_add_u32_dpp v11, v11, v11 row_mirror row_mask:0xf bank_mask:0xf bound_ctrl:1
	v_add_u32_dpp v12, v12, v12 row_mirror row_mask:0xf bank_mask:0xf bound_ctrl:1
	v_add_u32_dpp v13, v13, v13 row_mirror row_mask:0xf bank_mask:0xf bound_ctrl:1
	v_add_u32_dpp v14, v14, v14 row_mirror row_mask:0xf bank_mask:0xf bound_ctrl:1
	v_add_u32_dpp v15, v15, v15 row_mirror row_mask:0xf bank_mask:0xf bound_ctrl:1
	v_add_u32_dpp v16, v16, v16 row_mirror row_mask:0xf bank_mask:0xf bound_ctrl:1
	v_add_u32_dpp v17, v17, v17 row_mirror row_mask:0xf bank_mask:0xf bound_ctrl:1
	v_add_u32_dpp v18, v18, v18 row_mirror row_mask:0xf bank_mask:0xf bound_ctrl:1
	v_add_u32_dpp v19, v19, v19 row_mirror row_mask:0xf bank_mask:0xf bound_ctrl:1
	v_add_u32_dpp v20, v20, v20 row_mirror row_mask:0xf bank_mask:0xf bound_ctrl:1
	v_add_u32_dpp v21, v21, v21 row_mirror row_mask:0xf bank_mask:0xf bound_ctrl:1
	v_add_u32_dpp v22, v22, v22 row_mirror row_mask:0xf bank_mask:0xf bound_ctrl:1
	v_add_u32_dpp v23, v23, v23 row_mirror row_mask:0xf bank_mask:0xf bound_ctrl:1
	v_mov_b32_dpp v24, v8 row_bcast:15 row_mask:0xa bank_mask:0xf bound_ctrl:1
	v_mov_b32_dpp v25, v9 row_bcast:15 row_mask:0xa bank_mask:0xf bound_ctrl:1
	v_mov_b32_dpp v26, v10 row_bcast:15 row_mask:0xa bank_mask:0xf bound_ctrl:1
	v_mov_b32_dpp v27, v11 row_bcast:15 row_mask:0xa bank_mask:0xf bound_ctrl:1
	v_mov_b32_dpp v28, v12 row_bcast:15 row_mask:0xa bank_mask:0xf bound_ctrl:1
	v_mov_b32_dpp v29, v13 row_bcast:15 row_mask:0xa bank_mask:0xf bound_ctrl:1
	v_mov_b32_dpp v30, v14 row_bcast:15 row_mask:0xa bank_mask:0xf bound_ctrl:1
	v_mov_b32_dpp v31, v15 row_bcast:15 row_mask:0xa bank_mask:0xf bound_ctrl:1
	v_mov_b32_dpp v32, v16 row_bcast:15 row_mask:0xa bank_mask:0xf bound_ctrl:1
	v_mov_b32_dpp v33, v17 row_bcast:15 row_mask:0xa bank_mask:0xf bound_ctrl:1
	v_mov_b32_dpp v130, v18 row_bcast:15 row_mask:0xa bank_mask:0xf bound_ctrl:1
	v_mov_b32_dpp v131, v19 row_bcast:15 row_mask:0xa bank_mask:0xf bound_ctrl:1
	v_mov_b32_dpp v132, v20 row_bcast:15 row_mask:0xa bank_mask:0xf bound_ctrl:1
	v_mov_b32_dpp v133, v21 row_bcast:15 row_mask:0xa bank_mask:0xf bound_ctrl:1
	v_mov_b32_dpp v134, v22 row_bcast:15 row_mask:0xa bank_mask:0xf bound_ctrl:1
	v_mov_b32_dpp v135, v23 row_bcast:15 row_mask:0xa bank_mask:0xf bound_ctrl:1
	s_and_saveexec_b64 s[36:37], vcc
	v_add_u32_e32 v8, v8, v24
	v_add_u32_e32 v9, v9, v25
	v_add_u32_e32 v10, v10, v26
	v_add_u32_e32 v11, v11, v27
	v_add_u32_e32 v12, v12, v28
	v_add_u32_e32 v13, v13, v29
	v_add_u32_e32 v14, v14, v30
	v_add_u32_e32 v15, v15, v31
	v_add_u32_e32 v16, v16, v32
	v_add_u32_e32 v17, v17, v33
	v_add_u32_e32 v18, v18, v130
	v_add_u32_e32 v19, v19, v131
	v_add_u32_e32 v20, v20, v132
	v_add_u32_e32 v21, v21, v133
	v_add_u32_e32 v22, v22, v134
	v_add_u32_e32 v23, v23, v135
	v_cvt_f32_u32_sdwa v24, v8 dst_sel:DWORD dst_unused:UNUSED_PAD src0_sel:WORD_0
	v_cvt_f32_u32_sdwa v25, v8 dst_sel:DWORD dst_unused:UNUSED_PAD src0_sel:WORD_1
	v_cvt_f32_u32_sdwa v26, v16 dst_sel:DWORD dst_unused:UNUSED_PAD src0_sel:WORD_0
	v_cvt_f32_u32_sdwa v27, v16 dst_sel:DWORD dst_unused:UNUSED_PAD src0_sel:WORD_1
	v_cvt_f32_u32_sdwa v28, v9 dst_sel:DWORD dst_unused:UNUSED_PAD src0_sel:WORD_0
	v_cvt_f32_u32_sdwa v29, v9 dst_sel:DWORD dst_unused:UNUSED_PAD src0_sel:WORD_1
	v_cvt_f32_u32_sdwa v30, v17 dst_sel:DWORD dst_unused:UNUSED_PAD src0_sel:WORD_0
	v_cvt_f32_u32_sdwa v31, v17 dst_sel:DWORD dst_unused:UNUSED_PAD src0_sel:WORD_1
	v_cvt_f32_u32_sdwa v32, v10 dst_sel:DWORD dst_unused:UNUSED_PAD src0_sel:WORD_0
	v_cvt_f32_u32_sdwa v33, v10 dst_sel:DWORD dst_unused:UNUSED_PAD src0_sel:WORD_1
	v_cvt_f32_u32_sdwa v130, v18 dst_sel:DWORD dst_unused:UNUSED_PAD src0_sel:WORD_0
	v_cvt_f32_u32_sdwa v131, v18 dst_sel:DWORD dst_unused:UNUSED_PAD src0_sel:WORD_1
	v_cvt_f32_u32_sdwa v132, v11 dst_sel:DWORD dst_unused:UNUSED_PAD src0_sel:WORD_0
	v_cvt_f32_u32_sdwa v133, v11 dst_sel:DWORD dst_unused:UNUSED_PAD src0_sel:WORD_1
	v_cvt_f32_u32_sdwa v134, v19 dst_sel:DWORD dst_unused:UNUSED_PAD src0_sel:WORD_0
	v_cvt_f32_u32_sdwa v135, v19 dst_sel:DWORD dst_unused:UNUSED_PAD src0_sel:WORD_1
	v_cvt_f32_u32_sdwa v136, v12 dst_sel:DWORD dst_unused:UNUSED_PAD src0_sel:WORD_0
	v_cvt_f32_u32_sdwa v137, v12 dst_sel:DWORD dst_unused:UNUSED_PAD src0_sel:WORD_1
	v_cvt_f32_u32_sdwa v138, v20 dst_sel:DWORD dst_unused:UNUSED_PAD src0_sel:WORD_0
	v_cvt_f32_u32_sdwa v139, v20 dst_sel:DWORD dst_unused:UNUSED_PAD src0_sel:WORD_1
	v_cvt_f32_u32_sdwa v140, v13 dst_sel:DWORD dst_unused:UNUSED_PAD src0_sel:WORD_0
	v_cvt_f32_u32_sdwa v141, v13 dst_sel:DWORD dst_unused:UNUSED_PAD src0_sel:WORD_1
	v_cvt_f32_u32_sdwa v142, v21 dst_sel:DWORD dst_unused:UNUSED_PAD src0_sel:WORD_0
	v_cvt_f32_u32_sdwa v143, v21 dst_sel:DWORD dst_unused:UNUSED_PAD src0_sel:WORD_1
	v_cvt_f32_u32_sdwa v144, v14 dst_sel:DWORD dst_unused:UNUSED_PAD src0_sel:WORD_0
	v_cvt_f32_u32_sdwa v145, v14 dst_sel:DWORD dst_unused:UNUSED_PAD src0_sel:WORD_1
	v_cvt_f32_u32_sdwa v146, v22 dst_sel:DWORD dst_unused:UNUSED_PAD src0_sel:WORD_0
	v_cvt_f32_u32_sdwa v147, v22 dst_sel:DWORD dst_unused:UNUSED_PAD src0_sel:WORD_1
	v_cvt_f32_u32_sdwa v148, v15 dst_sel:DWORD dst_unused:UNUSED_PAD src0_sel:WORD_0
	v_cvt_f32_u32_sdwa v149, v15 dst_sel:DWORD dst_unused:UNUSED_PAD src0_sel:WORD_1
	v_cvt_f32_u32_sdwa v150, v23 dst_sel:DWORD dst_unused:UNUSED_PAD src0_sel:WORD_0
	v_cvt_f32_u32_sdwa v151, v23 dst_sel:DWORD dst_unused:UNUSED_PAD src0_sel:WORD_1
	ds_write_b32 v152, v24 offset:236
	ds_write_b32 v152, v25 offset:108
	ds_write_b32 v152, v26 offset:172
	ds_write_b32 v152, v27 offset:44
	ds_write_b32 v152, v28 offset:232
	ds_write_b32 v152, v29 offset:104
	ds_write_b32 v152, v30 offset:168
	ds_write_b32 v152, v31 offset:40
	ds_write_b32 v152, v32 offset:228
	ds_write_b32 v152, v33 offset:100
	ds_write_b32 v152, v130 offset:164
	ds_write_b32 v152, v131 offset:36
	ds_write_b32 v152, v132 offset:224
	ds_write_b32 v152, v133 offset:96
	ds_write_b32 v152, v134 offset:160
	ds_write_b32 v152, v135 offset:32
	ds_write_b32 v152, v136 offset:204
	ds_write_b32 v152, v137 offset:76
	ds_write_b32 v152, v138 offset:140
	ds_write_b32 v152, v139 offset:12
	ds_write_b32 v152, v140 offset:200
	ds_write_b32 v152, v141 offset:72
	ds_write_b32 v152, v142 offset:136
	ds_write_b32 v152, v143 offset:8
	ds_write_b32 v152, v144 offset:196
	ds_write_b32 v152, v145 offset:68
	ds_write_b32 v152, v146 offset:132
	ds_write_b32 v152, v147 offset:4
	ds_write_b32 v152, v148 offset:192
	ds_write_b32 v152, v149 offset:64
	ds_write_b32 v152, v150 offset:128
	ds_write_b32 v152, v151
	s_or_b64 exec, exec, s[36:37]
	s_waitcnt vmcnt(6)
	v_mfma_scale_f32_32x32x64_f8f6f4 v[2:17], v[34:41], v[106:113], 0, v201, v201 op_sel_hi:[0,0,0]
	s_waitcnt vmcnt(4)
	v_mfma_scale_f32_32x32x64_f8f6f4 v[2:17], v[42:49], v[122:129], v[2:17], v201, v201 op_sel_hi:[0,0,0]
	s_waitcnt vmcnt(2)
	v_mfma_scale_f32_32x32x64_f8f6f4 v[2:17], v[50:57], v[114:121], v[2:17], v201, v201 op_sel_hi:[0,0,0]
	s_cmp_eq_u32 s52, 0
	s_cselect_b64 s[36:37], -1, 0
	s_and_b64 vcc, exec, s[36:37]
	s_waitcnt lgkmcnt(0)
	s_barrier
	s_cbranch_vccz .LBB1_93
	v_lshlrev_b32_e32 v32, 2, v194
	ds_read2st64_b32 v[18:19], v32 offset0:136 offset1:137
	ds_read2st64_b32 v[20:21], v32 offset0:128 offset1:129
	ds_read2st64_b32 v[22:23], v32 offset0:138 offset1:139
	ds_read2st64_b32 v[24:25], v32 offset0:140 offset1:141
	ds_read2st64_b32 v[26:27], v32 offset0:142 offset1:143
	ds_read2st64_b32 v[28:29], v32 offset0:130 offset1:131
	ds_read2st64_b32 v[30:31], v32 offset0:132 offset1:133
	ds_read2st64_b32 v[32:33], v32 offset0:134 offset1:135
	s_waitcnt lgkmcnt(7)
	v_add_f32_e32 v18, 0, v18
	s_waitcnt lgkmcnt(6)
	v_add_f32_e32 v20, 0, v20
	v_add_f32_e32 v18, v18, v19
	v_add_f32_e32 v19, v20, v21
	s_waitcnt lgkmcnt(2)
	v_add_f32_e32 v19, v19, v28
	v_add_f32_e32 v19, v19, v29
	s_waitcnt lgkmcnt(1)
	v_add_f32_e32 v19, v19, v30
	v_add_f32_e32 v19, v19, v31
	v_add_f32_e32 v18, v18, v22
	s_waitcnt lgkmcnt(0)
	v_add_f32_e32 v19, v19, v32
	v_lshrrev_b32_e32 v22, 1, v0
	v_add_f32_e32 v18, v18, v23
	v_add_f32_e32 v19, v19, v33
	v_lshlrev_b32_e32 v20, 4, v196
	v_and_b32_e32 v21, 3, v0
	v_and_b32_e32 v22, 12, v22
	v_add_f32_e32 v18, v18, v24
	v_or3_b32 v20, v20, v21, v22
	v_rcp_f32_e32 v22, v19
	v_add_f32_e32 v18, v18, v25
	v_add_f32_e32 v18, v18, v26
	v_lshlrev_b32_e32 v21, 5, v0
	v_lshlrev_b32_e32 v20, 2, v20
	s_movk_i32 s34, 0x80
	v_add_f32_e32 v18, v18, v27
	v_and_or_b32 v20, v21, s34, v20
	v_cmp_lt_f32_e32 vcc, 0, v19
	v_rcp_f32_e32 v18, v18
	s_nop 0
	v_min_f32_e32 v18, 0x4e800000, v18
	ds_write_b32 v20, v18 offset:37376
	s_nop 0
	v_cndmask_b32_e32 v18, 0, v22, vcc
	ds_write2st64_b32 v20, v19, v18 offset0:144 offset1:145
.LBB1_93:
	s_waitcnt vmcnt(0)
	v_mfma_scale_f32_32x32x64_f8f6f4 v[2:17], v[58:65], v[98:105], v[2:17], v201, v201 op_sel_hi:[0,0,0]
	v_lshlrev_b32_e32 v18, 7, v196
	s_waitcnt lgkmcnt(0)
	s_barrier
	ds_read_b128 v[162:165], v18 offset:37376
	ds_read_b128 v[166:169], v18 offset:37392
	ds_read_b128 v[170:173], v18 offset:37408
	ds_read_b128 v[174:177], v18 offset:37424
	ds_read_b128 v[178:181], v18 offset:37440
	ds_read_b128 v[182:185], v18 offset:37456
	ds_read_b128 v[186:189], v18 offset:37472
	ds_read_b128 v[190:193], v18 offset:37488
	s_lshl_b32 s34, s35, 3
	v_or_b32_e32 v202, 0x9100, v18
	s_add_i32 s38, s34, 16
	v_mov_b32_e32 v201, 0
	s_mov_b32 s39, -2
	v_mov_b32_e32 v203, 0x7f7f7f7f
	s_mov_b32 s39, 0
.Lq2_loop:
	s_lshl_b32 s34, s39, 2
	s_add_i32 s34, s34, s35
	s_and_b32 s41, s34, 15
	s_add_i32 s54, s34, 1
	s_and_b32 s54, s54, 15
	s_lshl_b32 s55, s41, 8
	s_lshl_b32 s38, s52, 12
	s_add_i32 s55, s55, s38
	v_lshl_add_u32 v236, v194, 2, s55
	ds_read_b32 v200, v236
	s_lshl_b32 s34, s54, 3
	s_add_i32 s34, s34, s52
	s_lshl_b32 s34, s34, 13
	s_add_i32 s34, s34, s53
	buffer_load_dwordx4 v[146:149], v195, s[44:47], s34 offen
	s_or_b32 s42, s34, 0x400
	buffer_load_dwordx4 v[150:153], v195, s[44:47], s42 offen
	s_or_b32 s43, s34, 0x800
	buffer_load_dwordx4 v[154:157], v195, s[44:47], s43 offen
	s_or_b32 s42, s34, 0xc00
	buffer_load_dwordx4 v[158:161], v195, s[44:47], s42 offen
	s_or_b32 s43, s34, 0x1000
	buffer_load_dwordx4 v[138:141], v195, s[44:47], s43 offen
	s_or_b32 s42, s34, 0x1400
	buffer_load_dwordx4 v[142:145], v195, s[44:47], s42 offen
	s_or_b32 s43, s34, 0x1800
	buffer_load_dwordx4 v[130:133], v195, s[44:47], s43 offen
	s_or_b32 s42, s34, 0x1c00
	buffer_load_dwordx4 v[134:137], v195, s[44:47], s42 offen
	s_lshl_b32 s55, s41, 3
	s_add_i32 s55, s55, s52
	s_cmp_lg_u32 s55, s33
	s_cbranch_scc1 .Lq2_nd0_0
	v_cndmask_b32_e64 v2, v2, v198, s[0:1]
	v_cndmask_b32_e64 v3, v3, v198, s[2:3]
	v_cndmask_b32_e64 v4, v4, v198, s[4:5]
	v_cndmask_b32_e64 v5, v5, v198, s[6:7]
	v_cndmask_b32_e64 v6, v6, v198, s[8:9]
	v_cndmask_b32_e64 v7, v7, v198, s[10:11]
	v_cndmask_b32_e64 v8, v8, v198, s[12:13]
	v_cndmask_b32_e64 v9, v9, v198, s[14:15]
	v_cndmask_b32_e64 v10, v10, v198, s[16:17]
	v_cndmask_b32_e64 v11, v11, v198, s[18:19]
	v_cndmask_b32_e64 v12, v12, v198, s[20:21]
	v_cndmask_b32_e64 v13, v13, v198, s[22:23]
	v_cndmask_b32_e64 v14, v14, v198, s[24:25]
	v_cndmask_b32_e64 v15, v15, v198, s[26:27]
	v_cndmask_b32_e64 v16, v16, v198, s[28:29]
	v_cndmask_b32_e64 v17, v17, v198, s[30:31]
.Lq2_nd0_0:
	v_mfma_scale_f32_32x32x64_f8f6f4 v[18:33], v[66:73], v[106:113], 0, v203, v203 op_sel_hi:[0,0,0]
	v_exp_f32_e64 v2, -v2
	v_exp_f32_e64 v3, -v3
	v_exp_f32_e64 v4, -v4
	v_exp_f32_e64 v5, -v5
	s_waitcnt lgkmcnt(0)
	v_add_co_u32_e64 v200, s[42:43], v200, v200
	v_add_co_u32_e64 v200, s[48:49], v200, v200
	v_add_co_u32_e64 v200, s[50:51], v200, v200
	v_add_co_u32_e64 v200, s[56:57], v200, v200
	v_add_f32_e32 v2, v2, v162
	v_add_f32_e32 v3, v3, v163
	v_add_f32_e32 v4, v4, v164
	v_add_f32_e32 v5, v5, v165
	v_cndmask_b32_e64 v204, 1.0, v2, s[42:43]
	v_cndmask_b32_e64 v205, 1.0, v3, s[48:49]
	v_cndmask_b32_e64 v206, 1.0, v4, s[50:51]
	v_cndmask_b32_e64 v207, 1.0, v5, s[56:57]
	v_mfma_scale_f32_32x32x64_f8f6f4 v[18:33], v[74:81], v[122:129], v[18:33], v203, v203 op_sel_hi:[0,0,0]
	v_exp_f32_e64 v6, -v6
	v_exp_f32_e64 v7, -v7
	v_exp_f32_e64 v8, -v8
	v_exp_f32_e64 v9, -v9
	v_add_co_u32_e64 v200, s[42:43], v200, v200
	v_add_co_u32_e64 v200, s[48:49], v200, v200
	v_add_co_u32_e64 v200, s[50:51], v200, v200
	v_add_co_u32_e64 v200, s[56:57], v200, v200
	v_add_f32_e32 v6, v6, v166
	v_add_f32_e32 v7, v7, v167
	v_add_f32_e32 v8, v8, v168
	v_add_f32_e32 v9, v9, v169
	v_cndmask_b32_e64 v208, 1.0, v6, s[42:43]
	v_cndmask_b32_e64 v209, 1.0, v7, s[48:49]
	v_cndmask_b32_e64 v210, 1.0, v8, s[50:51]
	v_cndmask_b32_e64 v211, 1.0, v9, s[56:57]
	v_mfma_scale_f32_32x32x64_f8f6f4 v[18:33], v[82:89], v[114:121], v[18:33], v203, v203 op_sel_hi:[0,0,0]
	v_exp_f32_e64 v10, -v10
	v_exp_f32_e64 v11, -v11
	v_exp_f32_e64 v12, -v12
	v_exp_f32_e64 v13, -v13
	v_add_co_u32_e64 v200, s[42:43], v200, v200
	v_add_co_u32_e64 v200, s[48:49], v200, v200
	v_add_co_u32_e64 v200, s[50:51], v200, v200
	v_add_co_u32_e64 v200, s[56:57], v200, v200
	v_add_f32_e32 v10, v10, v170
	v_add_f32_e32 v11, v11, v171
	v_add_f32_e32 v12, v12, v172
	v_add_f32_e32 v13, v13, v173
	v_cndmask_b32_e64 v212, 1.0, v10, s[42:43]
	v_cndmask_b32_e64 v213, 1.0, v11, s[48:49]
	v_cndmask_b32_e64 v214, 1.0, v12, s[50:51]
	v_cndmask_b32_e64 v215, 1.0, v13, s[56:57]
	v_mfma_scale_f32_32x32x64_f8f6f4 v[18:33], v[90:97], v[98:105], v[18:33], v203, v203 op_sel_hi:[0,0,0]
	v_exp_f32_e64 v14, -v14
	v_exp_f32_e64 v15, -v15
	v_exp_f32_e64 v16, -v16
	v_exp_f32_e64 v17, -v17
	v_add_co_u32_e64 v200, s[42:43], v200, v200
	v_add_co_u32_e64 v200, s[48:49], v200, v200
	v_add_co_u32_e64 v200, s[50:51], v200, v200
	v_add_co_u32_e64 v200, s[56:57], v200, v200
	v_add_f32_e32 v14, v14, v174
	v_add_f32_e32 v15, v15, v175
	v_add_f32_e32 v16, v16, v176
	v_add_f32_e32 v17, v17, v177
	v_cndmask_b32_e64 v216, 1.0, v14, s[42:43]
	v_cndmask_b32_e64 v217, 1.0, v15, s[48:49]
	v_cndmask_b32_e64 v218, 1.0, v16, s[50:51]
	v_cndmask_b32_e64 v219, 1.0, v17, s[56:57]
	s_cmp_lg_u32 s55, s40
	s_cbranch_scc1 .Lq2_nd1_0
	s_nop 15
	s_nop 7
	v_cndmask_b32_e64 v18, v18, v199, s[0:1]
	v_cndmask_b32_e64 v19, v19, v199, s[2:3]
	v_cndmask_b32_e64 v20, v20, v199, s[4:5]
	v_cndmask_b32_e64 v21, v21, v199, s[6:7]
	v_cndmask_b32_e64 v22, v22, v199, s[8:9]
	v_cndmask_b32_e64 v23, v23, v199, s[10:11]
	v_cndmask_b32_e64 v24, v24, v199, s[12:13]
	v_cndmask_b32_e64 v25, v25, v199, s[14:15]
	v_cndmask_b32_e64 v26, v26, v199, s[16:17]
	v_cndmask_b32_e64 v27, v27, v199, s[18:19]
	v_cndmask_b32_e64 v28, v28, v199, s[20:21]
	v_cndmask_b32_e64 v29, v29, v199, s[22:23]
	v_cndmask_b32_e64 v30, v30, v199, s[24:25]
	v_cndmask_b32_e64 v31, v31, v199, s[26:27]
	v_cndmask_b32_e64 v32, v32, v199, s[28:29]
	v_cndmask_b32_e64 v33, v33, v199, s[30:31]
.Lq2_nd1_0:
	s_nop 3
	s_waitcnt vmcnt(6)
	v_mfma_scale_f32_32x32x64_f8f6f4 v[2:17], v[34:41], v[146:153], 0, v203, v203 op_sel_hi:[0,0,0]
	v_exp_f32_e64 v18, -v18
	v_exp_f32_e64 v19, -v19
	v_exp_f32_e64 v20, -v20
	v_exp_f32_e64 v21, -v21
	v_add_co_u32_e64 v200, s[42:43], v200, v200
	v_add_co_u32_e64 v200, s[48:49], v200, v200
	v_add_co_u32_e64 v200, s[50:51], v200, v200
	v_add_co_u32_e64 v200, s[56:57], v200, v200
	v_add_f32_e32 v18, v18, v178
	v_add_f32_e32 v19, v19, v179
	v_add_f32_e32 v20, v20, v180
	v_add_f32_e32 v21, v21, v181
	v_cndmask_b32_e64 v220, 1.0, v18, s[42:43]
	v_cndmask_b32_e64 v221, 1.0, v19, s[48:49]
	v_cndmask_b32_e64 v222, 1.0, v20, s[50:51]
	v_cndmask_b32_e64 v223, 1.0, v21, s[56:57]
	s_waitcnt vmcnt(4)
	v_mfma_scale_f32_32x32x64_f8f6f4 v[2:17], v[42:49], v[154:161], v[2:17], v203, v203 op_sel_hi:[0,0,0]
	v_exp_f32_e64 v22, -v22
	v_exp_f32_e64 v23, -v23
	v_exp_f32_e64 v24, -v24
	v_exp_f32_e64 v25, -v25
	v_add_co_u32_e64 v200, s[42:43], v200, v200
	v_add_co_u32_e64 v200, s[48:49], v200, v200
	v_add_co_u32_e64 v200, s[50:51], v200, v200
	v_add_co_u32_e64 v200, s[56:57], v200, v200
	v_add_f32_e32 v22, v22, v182
	v_add_f32_e32 v23, v23, v183
	v_add_f32_e32 v24, v24, v184
	v_add_f32_e32 v25, v25, v185
	v_cndmask_b32_e64 v224, 1.0, v22, s[42:43]
	v_cndmask_b32_e64 v225, 1.0, v23, s[48:49]
	v_cndmask_b32_e64 v226, 1.0, v24, s[50:51]
	v_cndmask_b32_e64 v227, 1.0, v25, s[56:57]
	s_waitcnt vmcnt(2)
	v_mfma_scale_f32_32x32x64_f8f6f4 v[2:17], v[50:57], v[138:145], v[2:17], v203, v203 op_sel_hi:[0,0,0]
	v_exp_f32_e64 v26, -v26
	v_exp_f32_e64 v27, -v27
	v_exp_f32_e64 v28, -v28
	v_exp_f32_e64 v29, -v29
	v_add_co_u32_e64 v200, s[42:43], v200, v200
	v_add_co_u32_e64 v200, s[48:49], v200, v200
	v_add_co_u32_e64 v200, s[50:51], v200, v200
	v_add_co_u32_e64 v200, s[56:57], v200, v200
	v_add_f32_e32 v26, v26, v186
	v_add_f32_e32 v27, v27, v187
	v_add_f32_e32 v28, v28, v188
	v_add_f32_e32 v29, v29, v189
	v_cndmask_b32_e64 v228, 1.0, v26, s[42:43]
	v_cndmask_b32_e64 v229, 1.0, v27, s[48:49]
	v_cndmask_b32_e64 v230, 1.0, v28, s[50:51]
	v_cndmask_b32_e64 v231, 1.0, v29, s[56:57]
	s_waitcnt vmcnt(0)
	v_mfma_scale_f32_32x32x64_f8f6f4 v[2:17], v[58:65], v[130:137], v[2:17], v203, v203 op_sel_hi:[0,0,0]
	v_exp_f32_e64 v30, -v30
	v_exp_f32_e64 v31, -v31
	v_exp_f32_e64 v32, -v32
	v_exp_f32_e64 v33, -v33
	v_add_co_u32_e64 v200, s[42:43], v200, v200
	v_add_co_u32_e64 v200, s[48:49], v200, v200
	v_add_co_u32_e64 v200, s[50:51], v200, v200
	v_add_co_u32_e64 v200, s[56:57], v200, v200
	v_add_f32_e32 v30, v30, v190
	v_add_f32_e32 v31, v31, v191
	v_add_f32_e32 v32, v32, v192
	v_add_f32_e32 v33, v33, v193
	v_cndmask_b32_e64 v232, 1.0, v30, s[42:43]
	v_cndmask_b32_e64 v233, 1.0, v31, s[48:49]
	v_cndmask_b32_e64 v234, 1.0, v32, s[50:51]
	v_cndmask_b32_e64 v235, 1.0, v33, s[56:57]
	s_lshl_b32 s34, s39, 2
	s_add_i32 s34, s34, 1
	s_add_i32 s34, s34, s35
	s_and_b32 s41, s34, 15
	s_add_i32 s54, s34, 1
	s_and_b32 s54, s54, 15
	s_lshl_b32 s55, s41, 8
	s_lshl_b32 s38, s52, 12
	s_add_i32 s55, s55, s38
	v_lshl_add_u32 v236, v194, 2, s55
	ds_read_b32 v200, v236
	s_lshl_b32 s34, s54, 3
	s_add_i32 s34, s34, s52
	s_lshl_b32 s34, s34, 13
	s_add_i32 s34, s34, s53
	buffer_load_dwordx4 v[106:109], v195, s[44:47], s34 offen
	s_or_b32 s42, s34, 0x400
	buffer_load_dwordx4 v[110:113], v195, s[44:47], s42 offen
	s_or_b32 s43, s34, 0x800
	buffer_load_dwordx4 v[122:125], v195, s[44:47], s43 offen
	s_or_b32 s42, s34, 0xc00
	buffer_load_dwordx4 v[126:129], v195, s[44:47], s42 offen
	s_or_b32 s43, s34, 0x1000
	buffer_load_dwordx4 v[114:117], v195, s[44:47], s43 offen
	s_or_b32 s42, s34, 0x1400
	buffer_load_dwordx4 v[118:121], v195, s[44:47], s42 offen
	s_or_b32 s43, s34, 0x1800
	buffer_load_dwordx4 v[98:101], v195, s[44:47], s43 offen
	s_or_b32 s42, s34, 0x1c00
	buffer_load_dwordx4 v[102:105], v195, s[44:47], s42 offen
	s_lshl_b32 s55, s41, 3
	s_add_i32 s55, s55, s52
	s_cmp_lg_u32 s55, s33
	s_cbranch_scc1 .Lq2_nd0_1
	v_cndmask_b32_e64 v2, v2, v198, s[0:1]
	v_cndmask_b32_e64 v3, v3, v198, s[2:3]
	v_cndmask_b32_e64 v4, v4, v198, s[4:5]
	v_cndmask_b32_e64 v5, v5, v198, s[6:7]
	v_cndmask_b32_e64 v6, v6, v198, s[8:9]
	v_cndmask_b32_e64 v7, v7, v198, s[10:11]
	v_cndmask_b32_e64 v8, v8, v198, s[12:13]
	v_cndmask_b32_e64 v9, v9, v198, s[14:15]
	v_cndmask_b32_e64 v10, v10, v198, s[16:17]
	v_cndmask_b32_e64 v11, v11, v198, s[18:19]
	v_cndmask_b32_e64 v12, v12, v198, s[20:21]
	v_cndmask_b32_e64 v13, v13, v198, s[22:23]
	v_cndmask_b32_e64 v14, v14, v198, s[24:25]
	v_cndmask_b32_e64 v15, v15, v198, s[26:27]
	v_cndmask_b32_e64 v16, v16, v198, s[28:29]
	v_cndmask_b32_e64 v17, v17, v198, s[30:31]
.Lq2_nd0_1:
	v_mfma_scale_f32_32x32x64_f8f6f4 v[18:33], v[66:73], v[146:153], 0, v203, v203 op_sel_hi:[0,0,0]
	v_exp_f32_e64 v2, -v2
	v_exp_f32_e64 v3, -v3
	v_exp_f32_e64 v4, -v4
	v_exp_f32_e64 v5, -v5
	s_waitcnt lgkmcnt(0)
	v_add_co_u32_e64 v200, s[42:43], v200, v200
	v_add_co_u32_e64 v200, s[48:49], v200, v200
	v_add_co_u32_e64 v200, s[50:51], v200, v200
	v_add_co_u32_e64 v200, s[56:57], v200, v200
	v_add_f32_e32 v2, v2, v162
	v_add_f32_e32 v3, v3, v163
	v_add_f32_e32 v4, v4, v164
	v_add_f32_e32 v5, v5, v165
	v_cndmask_b32_e64 v2, 1.0, v2, s[42:43]
	v_cndmask_b32_e64 v3, 1.0, v3, s[48:49]
	v_cndmask_b32_e64 v4, 1.0, v4, s[50:51]
	v_cndmask_b32_e64 v5, 1.0, v5, s[56:57]
	v_mul_f32_e32 v204, v204, v2
	v_mul_f32_e32 v205, v205, v3
	v_mul_f32_e32 v206, v206, v4
	v_mul_f32_e32 v207, v207, v5
	v_mfma_scale_f32_32x32x64_f8f6f4 v[18:33], v[74:81], v[154:161], v[18:33], v203, v203 op_sel_hi:[0,0,0]
	v_exp_f32_e64 v6, -v6
	v_exp_f32_e64 v7, -v7
	v_exp_f32_e64 v8, -v8
	v_exp_f32_e64 v9, -v9
	v_add_co_u32_e64 v200, s[42:43], v200, v200
	v_add_co_u32_e64 v200, s[48:49], v200, v200
	v_add_co_u32_e64 v200, s[50:51], v200, v200
	v_add_co_u32_e64 v200, s[56:57], v200, v200
	v_add_f32_e32 v6, v6, v166
	v_add_f32_e32 v7, v7, v167
	v_add_f32_e32 v8, v8, v168
	v_add_f32_e32 v9, v9, v169
	v_cndmask_b32_e64 v6, 1.0, v6, s[42:43]
	v_cndmask_b32_e64 v7, 1.0, v7, s[48:49]
	v_cndmask_b32_e64 v8, 1.0, v8, s[50:51]
	v_cndmask_b32_e64 v9, 1.0, v9, s[56:57]
	v_mul_f32_e32 v208, v208, v6
	v_mul_f32_e32 v209, v209, v7
	v_mul_f32_e32 v210, v210, v8
	v_mul_f32_e32 v211, v211, v9
	v_mfma_scale_f32_32x32x64_f8f6f4 v[18:33], v[82:89], v[138:145], v[18:33], v203, v203 op_sel_hi:[0,0,0]
	v_exp_f32_e64 v10, -v10
	v_exp_f32_e64 v11, -v11
	v_exp_f32_e64 v12, -v12
	v_exp_f32_e64 v13, -v13
	v_add_co_u32_e64 v200, s[42:43], v200, v200
	v_add_co_u32_e64 v200, s[48:49], v200, v200
	v_add_co_u32_e64 v200, s[50:51], v200, v200
	v_add_co_u32_e64 v200, s[56:57], v200, v200
	v_add_f32_e32 v10, v10, v170
	v_add_f32_e32 v11, v11, v171
	v_add_f32_e32 v12, v12, v172
	v_add_f32_e32 v13, v13, v173
	v_cndmask_b32_e64 v10, 1.0, v10, s[42:43]
	v_cndmask_b32_e64 v11, 1.0, v11, s[48:49]
	v_cndmask_b32_e64 v12, 1.0, v12, s[50:51]
	v_cndmask_b32_e64 v13, 1.0, v13, s[56:57]
	v_mul_f32_e32 v212, v212, v10
	v_mul_f32_e32 v213, v213, v11
	v_mul_f32_e32 v214, v214, v12
	v_mul_f32_e32 v215, v215, v13
	v_mfma_scale_f32_32x32x64_f8f6f4 v[18:33], v[90:97], v[130:137], v[18:33], v203, v203 op_sel_hi:[0,0,0]
	v_exp_f32_e64 v14, -v14
	v_exp_f32_e64 v15, -v15
	v_exp_f32_e64 v16, -v16
	v_exp_f32_e64 v17, -v17
	v_add_co_u32_e64 v200, s[42:43], v200, v200
	v_add_co_u32_e64 v200, s[48:49], v200, v200
	v_add_co_u32_e64 v200, s[50:51], v200, v200
	v_add_co_u32_e64 v200, s[56:57], v200, v200
	v_add_f32_e32 v14, v14, v174
	v_add_f32_e32 v15, v15, v175
	v_add_f32_e32 v16, v16, v176
	v_add_f32_e32 v17, v17, v177
	v_cndmask_b32_e64 v14, 1.0, v14, s[42:43]
	v_cndmask_b32_e64 v15, 1.0, v15, s[48:49]
	v_cndmask_b32_e64 v16, 1.0, v16, s[50:51]
	v_cndmask_b32_e64 v17, 1.0, v17, s[56:57]
	v_mul_f32_e32 v216, v216, v14
	v_mul_f32_e32 v217, v217, v15
	v_mul_f32_e32 v218, v218, v16
	v_mul_f32_e32 v219, v219, v17
	s_cmp_lg_u32 s55, s40
	s_cbranch_scc1 .Lq2_nd1_1
	s_nop 15
	s_nop 7
	v_cndmask_b32_e64 v18, v18, v199, s[0:1]
	v_cndmask_b32_e64 v19, v19, v199, s[2:3]
	v_cndmask_b32_e64 v20, v20, v199, s[4:5]
	v_cndmask_b32_e64 v21, v21, v199, s[6:7]
	v_cndmask_b32_e64 v22, v22, v199, s[8:9]
	v_cndmask_b32_e64 v23, v23, v199, s[10:11]
	v_cndmask_b32_e64 v24, v24, v199, s[12:13]
	v_cndmask_b32_e64 v25, v25, v199, s[14:15]
	v_cndmask_b32_e64 v26, v26, v199, s[16:17]
	v_cndmask_b32_e64 v27, v27, v199, s[18:19]
	v_cndmask_b32_e64 v28, v28, v199, s[20:21]
	v_cndmask_b32_e64 v29, v29, v199, s[22:23]
	v_cndmask_b32_e64 v30, v30, v199, s[24:25]
	v_cndmask_b32_e64 v31, v31, v199, s[26:27]
	v_cndmask_b32_e64 v32, v32, v199, s[28:29]
	v_cndmask_b32_e64 v33, v33, v199, s[30:31]
.Lq2_nd1_1:
	s_nop 3
	s_waitcnt vmcnt(6)
	v_mfma_scale_f32_32x32x64_f8f6f4 v[2:17], v[34:41], v[106:113], 0, v203, v203 op_sel_hi:[0,0,0]
	v_exp_f32_e64 v18, -v18
	v_exp_f32_e64 v19, -v19
	v_exp_f32_e64 v20, -v20
	v_exp_f32_e64 v21, -v21
	v_add_co_u32_e64 v200, s[42:43], v200, v200
	v_add_co_u32_e64 v200, s[48:49], v200, v200
	v_add_co_u32_e64 v200, s[50:51], v200, v200
	v_add_co_u32_e64 v200, s[56:57], v200, v200
	v_add_f32_e32 v18, v18, v178
	v_add_f32_e32 v19, v19, v179
	v_add_f32_e32 v20, v20, v180
	v_add_f32_e32 v21, v21, v181
	v_cndmask_b32_e64 v18, 1.0, v18, s[42:43]
	v_cndmask_b32_e64 v19, 1.0, v19, s[48:49]
	v_cndmask_b32_e64 v20, 1.0, v20, s[50:51]
	v_cndmask_b32_e64 v21, 1.0, v21, s[56:57]
	v_mul_f32_e32 v220, v220, v18
	v_mul_f32_e32 v221, v221, v19
	v_mul_f32_e32 v222, v222, v20
	v_mul_f32_e32 v223, v223, v21
	s_waitcnt vmcnt(4)
	v_mfma_scale_f32_32x32x64_f8f6f4 v[2:17], v[42:49], v[122:129], v[2:17], v203, v203 op_sel_hi:[0,0,0]
	v_exp_f32_e64 v22, -v22
	v_exp_f32_e64 v23, -v23
	v_exp_f32_e64 v24, -v24
	v_exp_f32_e64 v25, -v25
	v_add_co_u32_e64 v200, s[42:43], v200, v200
	v_add_co_u32_e64 v200, s[48:49], v200, v200
	v_add_co_u32_e64 v200, s[50:51], v200, v200
	v_add_co_u32_e64 v200, s[56:57], v200, v200
	v_add_f32_e32 v22, v22, v182
	v_add_f32_e32 v23, v23, v183
	v_add_f32_e32 v24, v24, v184
	v_add_f32_e32 v25, v25, v185
	v_cndmask_b32_e64 v22, 1.0, v22, s[42:43]
	v_cndmask_b32_e64 v23, 1.0, v23, s[48:49]
	v_cndmask_b32_e64 v24, 1.0, v24, s[50:51]
	v_cndmask_b32_e64 v25, 1.0, v25, s[56:57]
	v_mul_f32_e32 v224, v224, v22
	v_mul_f32_e32 v225, v225, v23
	v_mul_f32_e32 v226, v226, v24
	v_mul_f32_e32 v227, v227, v25
	s_waitcnt vmcnt(2)
	v_mfma_scale_f32_32x32x64_f8f6f4 v[2:17], v[50:57], v[114:121], v[2:17], v203, v203 op_sel_hi:[0,0,0]
	v_exp_f32_e64 v26, -v26
	v_exp_f32_e64 v27, -v27
	v_exp_f32_e64 v28, -v28
	v_exp_f32_e64 v29, -v29
	v_add_co_u32_e64 v200, s[42:43], v200, v200
	v_add_co_u32_e64 v200, s[48:49], v200, v200
	v_add_co_u32_e64 v200, s[50:51], v200, v200
	v_add_co_u32_e64 v200, s[56:57], v200, v200
	v_add_f32_e32 v26, v26, v186
	v_add_f32_e32 v27, v27, v187
	v_add_f32_e32 v28, v28, v188
	v_add_f32_e32 v29, v29, v189
	v_cndmask_b32_e64 v26, 1.0, v26, s[42:43]
	v_cndmask_b32_e64 v27, 1.0, v27, s[48:49]
	v_cndmask_b32_e64 v28, 1.0, v28, s[50:51]
	v_cndmask_b32_e64 v29, 1.0, v29, s[56:57]
	v_mul_f32_e32 v228, v228, v26
	v_mul_f32_e32 v229, v229, v27
	v_mul_f32_e32 v230, v230, v28
	v_mul_f32_e32 v231, v231, v29
	s_waitcnt vmcnt(0)
	v_mfma_scale_f32_32x32x64_f8f6f4 v[2:17], v[58:65], v[98:105], v[2:17], v203, v203 op_sel_hi:[0,0,0]
	v_exp_f32_e64 v30, -v30
	v_exp_f32_e64 v31, -v31
	v_exp_f32_e64 v32, -v32
	v_exp_f32_e64 v33, -v33
	v_add_co_u32_e64 v200, s[42:43], v200, v200
	v_add_co_u32_e64 v200, s[48:49], v200, v200
	v_add_co_u32_e64 v200, s[50:51], v200, v200
	v_add_co_u32_e64 v200, s[56:57], v200, v200
	v_add_f32_e32 v30, v30, v190
	v_add_f32_e32 v31, v31, v191
	v_add_f32_e32 v32, v32, v192
	v_add_f32_e32 v33, v33, v193
	v_cndmask_b32_e64 v30, 1.0, v30, s[42:43]
	v_cndmask_b32_e64 v31, 1.0, v31, s[48:49]
	v_cndmask_b32_e64 v32, 1.0, v32, s[50:51]
	v_cndmask_b32_e64 v33, 1.0, v33, s[56:57]
	v_mul_f32_e32 v232, v232, v30
	v_mul_f32_e32 v233, v233, v31
	v_mul_f32_e32 v234, v234, v32
	v_mul_f32_e32 v235, v235, v33
	s_lshl_b32 s34, s39, 2
	s_add_i32 s34, s34, 2
	s_add_i32 s34, s34, s35
	s_and_b32 s41, s34, 15
	s_add_i32 s54, s34, 1
	s_and_b32 s54, s54, 15
	s_lshl_b32 s55, s41, 8
	s_lshl_b32 s38, s52, 12
	s_add_i32 s55, s55, s38
	v_lshl_add_u32 v236, v194, 2, s55
	ds_read_b32 v200, v236
	s_lshl_b32 s34, s54, 3
	s_add_i32 s34, s34, s52
	s_lshl_b32 s34, s34, 13
	s_add_i32 s34, s34, s53
	buffer_load_dwordx4 v[146:149], v195, s[44:47], s34 offen
	s_or_b32 s42, s34, 0x400
	buffer_load_dwordx4 v[150:153], v195, s[44:47], s42 offen
	s_or_b32 s43, s34, 0x800
	buffer_load_dwordx4 v[154:157], v195, s[44:47], s43 offen
	s_or_b32 s42, s34, 0xc00
	buffer_load_dwordx4 v[158:161], v195, s[44:47], s42 offen
	s_or_b32 s43, s34, 0x1000
	buffer_load_dwordx4 v[138:141], v195, s[44:47], s43 offen
	s_or_b32 s42, s34, 0x1400
	buffer_load_dwordx4 v[142:145], v195, s[44:47], s42 offen
	s_or_b32 s43, s34, 0x1800
	buffer_load_dwordx4 v[130:133], v195, s[44:47], s43 offen
	s_or_b32 s42, s34, 0x1c00
	buffer_load_dwordx4 v[134:137], v195, s[44:47], s42 offen
	s_lshl_b32 s55, s41, 3
	s_add_i32 s55, s55, s52
	s_cmp_lg_u32 s55, s33
	s_cbranch_scc1 .Lq2_nd0_2
	v_cndmask_b32_e64 v2, v2, v198, s[0:1]
	v_cndmask_b32_e64 v3, v3, v198, s[2:3]
	v_cndmask_b32_e64 v4, v4, v198, s[4:5]
	v_cndmask_b32_e64 v5, v5, v198, s[6:7]
	v_cndmask_b32_e64 v6, v6, v198, s[8:9]
	v_cndmask_b32_e64 v7, v7, v198, s[10:11]
	v_cndmask_b32_e64 v8, v8, v198, s[12:13]
	v_cndmask_b32_e64 v9, v9, v198, s[14:15]
	v_cndmask_b32_e64 v10, v10, v198, s[16:17]
	v_cndmask_b32_e64 v11, v11, v198, s[18:19]
	v_cndmask_b32_e64 v12, v12, v198, s[20:21]
	v_cndmask_b32_e64 v13, v13, v198, s[22:23]
	v_cndmask_b32_e64 v14, v14, v198, s[24:25]
	v_cndmask_b32_e64 v15, v15, v198, s[26:27]
	v_cndmask_b32_e64 v16, v16, v198, s[28:29]
	v_cndmask_b32_e64 v17, v17, v198, s[30:31]
.Lq2_nd0_2:
	v_mfma_scale_f32_32x32x64_f8f6f4 v[18:33], v[66:73], v[106:113], 0, v203, v203 op_sel_hi:[0,0,0]
	v_exp_f32_e64 v2, -v2
	v_exp_f32_e64 v3, -v3
	v_exp_f32_e64 v4, -v4
	v_exp_f32_e64 v5, -v5
	s_waitcnt lgkmcnt(0)
	v_add_co_u32_e64 v200, s[42:43], v200, v200
	v_add_co_u32_e64 v200, s[48:49], v200, v200
	v_add_co_u32_e64 v200, s[50:51], v200, v200
	v_add_co_u32_e64 v200, s[56:57], v200, v200
	v_add_f32_e32 v2, v2, v162
	v_add_f32_e32 v3, v3, v163
	v_add_f32_e32 v4, v4, v164
	v_add_f32_e32 v5, v5, v165
	v_cndmask_b32_e64 v2, 1.0, v2, s[42:43]
	v_cndmask_b32_e64 v3, 1.0, v3, s[48:49]
	v_cndmask_b32_e64 v4, 1.0, v4, s[50:51]
	v_cndmask_b32_e64 v5, 1.0, v5, s[56:57]
	v_mul_f32_e32 v204, v204, v2
	v_mul_f32_e32 v205, v205, v3
	v_mul_f32_e32 v206, v206, v4
	v_mul_f32_e32 v207, v207, v5
	v_mfma_scale_f32_32x32x64_f8f6f4 v[18:33], v[74:81], v[122:129], v[18:33], v203, v203 op_sel_hi:[0,0,0]
	v_exp_f32_e64 v6, -v6
	v_exp_f32_e64 v7, -v7
	v_exp_f32_e64 v8, -v8
	v_exp_f32_e64 v9, -v9
	v_add_co_u32_e64 v200, s[42:43], v200, v200
	v_add_co_u32_e64 v200, s[48:49], v200, v200
	v_add_co_u32_e64 v200, s[50:51], v200, v200
	v_add_co_u32_e64 v200, s[56:57], v200, v200
	v_add_f32_e32 v6, v6, v166
	v_add_f32_e32 v7, v7, v167
	v_add_f32_e32 v8, v8, v168
	v_add_f32_e32 v9, v9, v169
	v_cndmask_b32_e64 v6, 1.0, v6, s[42:43]
	v_cndmask_b32_e64 v7, 1.0, v7, s[48:49]
	v_cndmask_b32_e64 v8, 1.0, v8, s[50:51]
	v_cndmask_b32_e64 v9, 1.0, v9, s[56:57]
	v_mul_f32_e32 v208, v208, v6
	v_mul_f32_e32 v209, v209, v7
	v_mul_f32_e32 v210, v210, v8
	v_mul_f32_e32 v211, v211, v9
	v_mfma_scale_f32_32x32x64_f8f6f4 v[18:33], v[82:89], v[114:121], v[18:33], v203, v203 op_sel_hi:[0,0,0]
	v_exp_f32_e64 v10, -v10
	v_exp_f32_e64 v11, -v11
	v_exp_f32_e64 v12, -v12
	v_exp_f32_e64 v13, -v13
	v_add_co_u32_e64 v200, s[42:43], v200, v200
	v_add_co_u32_e64 v200, s[48:49], v200, v200
	v_add_co_u32_e64 v200, s[50:51], v200, v200
	v_add_co_u32_e64 v200, s[56:57], v200, v200
	v_add_f32_e32 v10, v10, v170
	v_add_f32_e32 v11, v11, v171
	v_add_f32_e32 v12, v12, v172
	v_add_f32_e32 v13, v13, v173
	v_cndmask_b32_e64 v10, 1.0, v10, s[42:43]
	v_cndmask_b32_e64 v11, 1.0, v11, s[48:49]
	v_cndmask_b32_e64 v12, 1.0, v12, s[50:51]
	v_cndmask_b32_e64 v13, 1.0, v13, s[56:57]
	v_mul_f32_e32 v212, v212, v10
	v_mul_f32_e32 v213, v213, v11
	v_mul_f32_e32 v214, v214, v12
	v_mul_f32_e32 v215, v215, v13
	v_mfma_scale_f32_32x32x64_f8f6f4 v[18:33], v[90:97], v[98:105], v[18:33], v203, v203 op_sel_hi:[0,0,0]
	v_exp_f32_e64 v14, -v14
	v_exp_f32_e64 v15, -v15
	v_exp_f32_e64 v16, -v16
	v_exp_f32_e64 v17, -v17
	v_add_co_u32_e64 v200, s[42:43], v200, v200
	v_add_co_u32_e64 v200, s[48:49], v200, v200
	v_add_co_u32_e64 v200, s[50:51], v200, v200
	v_add_co_u32_e64 v200, s[56:57], v200, v200
	v_add_f32_e32 v14, v14, v174
	v_add_f32_e32 v15, v15, v175
	v_add_f32_e32 v16, v16, v176
	v_add_f32_e32 v17, v17, v177
	v_cndmask_b32_e64 v14, 1.0, v14, s[42:43]
	v_cndmask_b32_e64 v15, 1.0, v15, s[48:49]
	v_cndmask_b32_e64 v16, 1.0, v16, s[50:51]
	v_cndmask_b32_e64 v17, 1.0, v17, s[56:57]
	v_mul_f32_e32 v216, v216, v14
	v_mul_f32_e32 v217, v217, v15
	v_mul_f32_e32 v218, v218, v16
	v_mul_f32_e32 v219, v219, v17
	s_cmp_lg_u32 s55, s40
	s_cbranch_scc1 .Lq2_nd1_2
	s_nop 15
	s_nop 7
	v_cndmask_b32_e64 v18, v18, v199, s[0:1]
	v_cndmask_b32_e64 v19, v19, v199, s[2:3]
	v_cndmask_b32_e64 v20, v20, v199, s[4:5]
	v_cndmask_b32_e64 v21, v21, v199, s[6:7]
	v_cndmask_b32_e64 v22, v22, v199, s[8:9]
	v_cndmask_b32_e64 v23, v23, v199, s[10:11]
	v_cndmask_b32_e64 v24, v24, v199, s[12:13]
	v_cndmask_b32_e64 v25, v25, v199, s[14:15]
	v_cndmask_b32_e64 v26, v26, v199, s[16:17]
	v_cndmask_b32_e64 v27, v27, v199, s[18:19]
	v_cndmask_b32_e64 v28, v28, v199, s[20:21]
	v_cndmask_b32_e64 v29, v29, v199, s[22:23]
	v_cndmask_b32_e64 v30, v30, v199, s[24:25]
	v_cndmask_b32_e64 v31, v31, v199, s[26:27]
	v_cndmask_b32_e64 v32, v32, v199, s[28:29]
	v_cndmask_b32_e64 v33, v33, v199, s[30:31]
.Lq2_nd1_2:
	s_nop 3
	s_waitcnt vmcnt(6)
	v_mfma_scale_f32_32x32x64_f8f6f4 v[2:17], v[34:41], v[146:153], 0, v203, v203 op_sel_hi:[0,0,0]
	v_exp_f32_e64 v18, -v18
	v_exp_f32_e64 v19, -v19
	v_exp_f32_e64 v20, -v20
	v_exp_f32_e64 v21, -v21
	v_add_co_u32_e64 v200, s[42:43], v200, v200
	v_add_co_u32_e64 v200, s[48:49], v200, v200
	v_add_co_u32_e64 v200, s[50:51], v200, v200
	v_add_co_u32_e64 v200, s[56:57], v200, v200
	v_add_f32_e32 v18, v18, v178
	v_add_f32_e32 v19, v19, v179
	v_add_f32_e32 v20, v20, v180
	v_add_f32_e32 v21, v21, v181
	v_cndmask_b32_e64 v18, 1.0, v18, s[42:43]
	v_cndmask_b32_e64 v19, 1.0, v19, s[48:49]
	v_cndmask_b32_e64 v20, 1.0, v20, s[50:51]
	v_cndmask_b32_e64 v21, 1.0, v21, s[56:57]
	v_mul_f32_e32 v220, v220, v18
	v_mul_f32_e32 v221, v221, v19
	v_mul_f32_e32 v222, v222, v20
	v_mul_f32_e32 v223, v223, v21
	s_waitcnt vmcnt(4)
	v_mfma_scale_f32_32x32x64_f8f6f4 v[2:17], v[42:49], v[154:161], v[2:17], v203, v203 op_sel_hi:[0,0,0]
	v_exp_f32_e64 v22, -v22
	v_exp_f32_e64 v23, -v23
	v_exp_f32_e64 v24, -v24
	v_exp_f32_e64 v25, -v25
	v_add_co_u32_e64 v200, s[42:43], v200, v200
	v_add_co_u32_e64 v200, s[48:49], v200, v200
	v_add_co_u32_e64 v200, s[50:51], v200, v200
	v_add_co_u32_e64 v200, s[56:57], v200, v200
	v_add_f32_e32 v22, v22, v182
	v_add_f32_e32 v23, v23, v183
	v_add_f32_e32 v24, v24, v184
	v_add_f32_e32 v25, v25, v185
	v_cndmask_b32_e64 v22, 1.0, v22, s[42:43]
	v_cndmask_b32_e64 v23, 1.0, v23, s[48:49]
	v_cndmask_b32_e64 v24, 1.0, v24, s[50:51]
	v_cndmask_b32_e64 v25, 1.0, v25, s[56:57]
	v_mul_f32_e32 v224, v224, v22
	v_mul_f32_e32 v225, v225, v23
	v_mul_f32_e32 v226, v226, v24
	v_mul_f32_e32 v227, v227, v25
	s_waitcnt vmcnt(2)
	v_mfma_scale_f32_32x32x64_f8f6f4 v[2:17], v[50:57], v[138:145], v[2:17], v203, v203 op_sel_hi:[0,0,0]
	v_exp_f32_e64 v26, -v26
	v_exp_f32_e64 v27, -v27
	v_exp_f32_e64 v28, -v28
	v_exp_f32_e64 v29, -v29
	v_add_co_u32_e64 v200, s[42:43], v200, v200
	v_add_co_u32_e64 v200, s[48:49], v200, v200
	v_add_co_u32_e64 v200, s[50:51], v200, v200
	v_add_co_u32_e64 v200, s[56:57], v200, v200
	v_add_f32_e32 v26, v26, v186
	v_add_f32_e32 v27, v27, v187
	v_add_f32_e32 v28, v28, v188
	v_add_f32_e32 v29, v29, v189
	v_cndmask_b32_e64 v26, 1.0, v26, s[42:43]
	v_cndmask_b32_e64 v27, 1.0, v27, s[48:49]
	v_cndmask_b32_e64 v28, 1.0, v28, s[50:51]
	v_cndmask_b32_e64 v29, 1.0, v29, s[56:57]
	v_mul_f32_e32 v228, v228, v26
	v_mul_f32_e32 v229, v229, v27
	v_mul_f32_e32 v230, v230, v28
	v_mul_f32_e32 v231, v231, v29
	s_waitcnt vmcnt(0)
	v_mfma_scale_f32_32x32x64_f8f6f4 v[2:17], v[58:65], v[130:137], v[2:17], v203, v203 op_sel_hi:[0,0,0]
	v_exp_f32_e64 v30, -v30
	v_exp_f32_e64 v31, -v31
	v_exp_f32_e64 v32, -v32
	v_exp_f32_e64 v33, -v33
	v_add_co_u32_e64 v200, s[42:43], v200, v200
	v_add_co_u32_e64 v200, s[48:49], v200, v200
	v_add_co_u32_e64 v200, s[50:51], v200, v200
	v_add_co_u32_e64 v200, s[56:57], v200, v200
	v_add_f32_e32 v30, v30, v190
	v_add_f32_e32 v31, v31, v191
	v_add_f32_e32 v32, v32, v192
	v_add_f32_e32 v33, v33, v193
	v_cndmask_b32_e64 v30, 1.0, v30, s[42:43]
	v_cndmask_b32_e64 v31, 1.0, v31, s[48:49]
	v_cndmask_b32_e64 v32, 1.0, v32, s[50:51]
	v_cndmask_b32_e64 v33, 1.0, v33, s[56:57]
	v_mul_f32_e32 v232, v232, v30
	v_mul_f32_e32 v233, v233, v31
	v_mul_f32_e32 v234, v234, v32
	v_mul_f32_e32 v235, v235, v33
	s_lshl_b32 s34, s39, 2
	s_add_i32 s34, s34, 3
	s_add_i32 s34, s34, s35
	s_and_b32 s41, s34, 15
	s_add_i32 s54, s34, 1
	s_and_b32 s54, s54, 15
	s_lshl_b32 s55, s41, 8
	s_lshl_b32 s38, s52, 12
	s_add_i32 s55, s55, s38
	v_lshl_add_u32 v236, v194, 2, s55
	ds_read_b32 v200, v236
	s_lshl_b32 s34, s54, 3
	s_add_i32 s34, s34, s52
	s_lshl_b32 s34, s34, 13
	s_add_i32 s34, s34, s53
	buffer_load_dwordx4 v[106:109], v195, s[44:47], s34 offen
	s_or_b32 s42, s34, 0x400
	buffer_load_dwordx4 v[110:113], v195, s[44:47], s42 offen
	s_or_b32 s43, s34, 0x800
	buffer_load_dwordx4 v[122:125], v195, s[44:47], s43 offen
	s_or_b32 s42, s34, 0xc00
	buffer_load_dwordx4 v[126:129], v195, s[44:47], s42 offen
	s_or_b32 s43, s34, 0x1000
	buffer_load_dwordx4 v[114:117], v195, s[44:47], s43 offen
	s_or_b32 s42, s34, 0x1400
	buffer_load_dwordx4 v[118:121], v195, s[44:47], s42 offen
	s_or_b32 s43, s34, 0x1800
	buffer_load_dwordx4 v[98:101], v195, s[44:47], s43 offen
	s_or_b32 s42, s34, 0x1c00
	buffer_load_dwordx4 v[102:105], v195, s[44:47], s42 offen
	s_lshl_b32 s55, s41, 3
	s_add_i32 s55, s55, s52
	s_cmp_lg_u32 s55, s33
	s_cbranch_scc1 .Lq2_nd0_3
	v_cndmask_b32_e64 v2, v2, v198, s[0:1]
	v_cndmask_b32_e64 v3, v3, v198, s[2:3]
	v_cndmask_b32_e64 v4, v4, v198, s[4:5]
	v_cndmask_b32_e64 v5, v5, v198, s[6:7]
	v_cndmask_b32_e64 v6, v6, v198, s[8:9]
	v_cndmask_b32_e64 v7, v7, v198, s[10:11]
	v_cndmask_b32_e64 v8, v8, v198, s[12:13]
	v_cndmask_b32_e64 v9, v9, v198, s[14:15]
	v_cndmask_b32_e64 v10, v10, v198, s[16:17]
	v_cndmask_b32_e64 v11, v11, v198, s[18:19]
	v_cndmask_b32_e64 v12, v12, v198, s[20:21]
	v_cndmask_b32_e64 v13, v13, v198, s[22:23]
	v_cndmask_b32_e64 v14, v14, v198, s[24:25]
	v_cndmask_b32_e64 v15, v15, v198, s[26:27]
	v_cndmask_b32_e64 v16, v16, v198, s[28:29]
	v_cndmask_b32_e64 v17, v17, v198, s[30:31]
.Lq2_nd0_3:
	v_mfma_scale_f32_32x32x64_f8f6f4 v[18:33], v[66:73], v[146:153], 0, v203, v203 op_sel_hi:[0,0,0]
	ds_read_b128 v[236:239], v202
	v_exp_f32_e64 v2, -v2
	v_exp_f32_e64 v3, -v3
	v_exp_f32_e64 v4, -v4
	v_exp_f32_e64 v5, -v5
	s_waitcnt lgkmcnt(1)
	v_add_co_u32_e64 v200, s[42:43], v200, v200
	v_add_co_u32_e64 v200, s[48:49], v200, v200
	v_add_co_u32_e64 v200, s[50:51], v200, v200
	v_add_co_u32_e64 v200, s[56:57], v200, v200
	v_add_f32_e32 v2, v2, v162
	v_add_f32_e32 v3, v3, v163
	v_add_f32_e32 v4, v4, v164
	v_add_f32_e32 v5, v5, v165
	v_cndmask_b32_e64 v2, 1.0, v2, s[42:43]
	v_cndmask_b32_e64 v3, 1.0, v3, s[48:49]
	v_cndmask_b32_e64 v4, 1.0, v4, s[50:51]
	v_cndmask_b32_e64 v5, 1.0, v5, s[56:57]
	v_mul_f32_e32 v2, v204, v2
	v_mul_f32_e32 v3, v205, v3
	v_mul_f32_e32 v4, v206, v4
	v_mul_f32_e32 v5, v207, v5
	v_log_f32_e32 v2, v2
	v_log_f32_e32 v3, v3
	v_log_f32_e32 v4, v4
	v_log_f32_e32 v5, v5
	s_waitcnt lgkmcnt(0)
	v_fmac_f32_e32 v201, v2, v236
	v_fmac_f32_e32 v201, v3, v237
	v_fmac_f32_e32 v201, v4, v238
	v_fmac_f32_e32 v201, v5, v239
	v_mfma_scale_f32_32x32x64_f8f6f4 v[18:33], v[74:81], v[154:161], v[18:33], v203, v203 op_sel_hi:[0,0,0]
	ds_read_b128 v[236:239], v202 offset:16
	v_exp_f32_e64 v6, -v6
	v_exp_f32_e64 v7, -v7
	v_exp_f32_e64 v8, -v8
	v_exp_f32_e64 v9, -v9
	v_add_co_u32_e64 v200, s[42:43], v200, v200
	v_add_co_u32_e64 v200, s[48:49], v200, v200
	v_add_co_u32_e64 v200, s[50:51], v200, v200
	v_add_co_u32_e64 v200, s[56:57], v200, v200
	v_add_f32_e32 v6, v6, v166
	v_add_f32_e32 v7, v7, v167
	v_add_f32_e32 v8, v8, v168
	v_add_f32_e32 v9, v9, v169
	v_cndmask_b32_e64 v6, 1.0, v6, s[42:43]
	v_cndmask_b32_e64 v7, 1.0, v7, s[48:49]
	v_cndmask_b32_e64 v8, 1.0, v8, s[50:51]
	v_cndmask_b32_e64 v9, 1.0, v9, s[56:57]
	v_mul_f32_e32 v6, v208, v6
	v_mul_f32_e32 v7, v209, v7
	v_mul_f32_e32 v8, v210, v8
	v_mul_f32_e32 v9, v211, v9
	v_log_f32_e32 v6, v6
	v_log_f32_e32 v7, v7
	v_log_f32_e32 v8, v8
	v_log_f32_e32 v9, v9
	s_waitcnt lgkmcnt(0)
	v_fmac_f32_e32 v201, v6, v236
	v_fmac_f32_e32 v201, v7, v237
	v_fmac_f32_e32 v201, v8, v238
	v_fmac_f32_e32 v201, v9, v239
	v_mfma_scale_f32_32x32x64_f8f6f4 v[18:33], v[82:89], v[138:145], v[18:33], v203, v203 op_sel_hi:[0,0,0]
	ds_read_b128 v[236:239], v202 offset:32
	v_exp_f32_e64 v10, -v10
	v_exp_f32_e64 v11, -v11
	v_exp_f32_e64 v12, -v12
	v_exp_f32_e64 v13, -v13
	v_add_co_u32_e64 v200, s[42:43], v200, v200
	v_add_co_u32_e64 v200, s[48:49], v200, v200
	v_add_co_u32_e64 v200, s[50:51], v200, v200
	v_add_co_u32_e64 v200, s[56:57], v200, v200
	v_add_f32_e32 v10, v10, v170
	v_add_f32_e32 v11, v11, v171
	v_add_f32_e32 v12, v12, v172
	v_add_f32_e32 v13, v13, v173
	v_cndmask_b32_e64 v10, 1.0, v10, s[42:43]
	v_cndmask_b32_e64 v11, 1.0, v11, s[48:49]
	v_cndmask_b32_e64 v12, 1.0, v12, s[50:51]
	v_cndmask_b32_e64 v13, 1.0, v13, s[56:57]
	v_mul_f32_e32 v10, v212, v10
	v_mul_f32_e32 v11, v213, v11
	v_mul_f32_e32 v12, v214, v12
	v_mul_f32_e32 v13, v215, v13
	v_log_f32_e32 v10, v10
	v_log_f32_e32 v11, v11
	v_log_f32_e32 v12, v12
	v_log_f32_e32 v13, v13
	s_waitcnt lgkmcnt(0)
	v_fmac_f32_e32 v201, v10, v236
	v_fmac_f32_e32 v201, v11, v237
	v_fmac_f32_e32 v201, v12, v238
	v_fmac_f32_e32 v201, v13, v239
	v_mfma_scale_f32_32x32x64_f8f6f4 v[18:33], v[90:97], v[130:137], v[18:33], v203, v203 op_sel_hi:[0,0,0]
	ds_read_b128 v[236:239], v202 offset:48
	v_exp_f32_e64 v14, -v14
	v_exp_f32_e64 v15, -v15
	v_exp_f32_e64 v16, -v16
	v_exp_f32_e64 v17, -v17
	v_add_co_u32_e64 v200, s[42:43], v200, v200
	v_add_co_u32_e64 v200, s[48:49], v200, v200
	v_add_co_u32_e64 v200, s[50:51], v200, v200
	v_add_co_u32_e64 v200, s[56:57], v200, v200
	v_add_f32_e32 v14, v14, v174
	v_add_f32_e32 v15, v15, v175
	v_add_f32_e32 v16, v16, v176
	v_add_f32_e32 v17, v17, v177
	v_cndmask_b32_e64 v14, 1.0, v14, s[42:43]
	v_cndmask_b32_e64 v15, 1.0, v15, s[48:49]
	v_cndmask_b32_e64 v16, 1.0, v16, s[50:51]
	v_cndmask_b32_e64 v17, 1.0, v17, s[56:57]
	v_mul_f32_e32 v14, v216, v14
	v_mul_f32_e32 v15, v217, v15
	v_mul_f32_e32 v16, v218, v16
	v_mul_f32_e32 v17, v219, v17
	v_log_f32_e32 v14, v14
	v_log_f32_e32 v15, v15
	v_log_f32_e32 v16, v16
	v_log_f32_e32 v17, v17
	s_waitcnt lgkmcnt(0)
	v_fmac_f32_e32 v201, v14, v236
	v_fmac_f32_e32 v201, v15, v237
	v_fmac_f32_e32 v201, v16, v238
	v_fmac_f32_e32 v201, v17, v239
	s_cmp_lg_u32 s55, s40
	s_cbranch_scc1 .Lq2_nd1_3
	s_nop 15
	s_nop 7
	v_cndmask_b32_e64 v18, v18, v199, s[0:1]
	v_cndmask_b32_e64 v19, v19, v199, s[2:3]
	v_cndmask_b32_e64 v20, v20, v199, s[4:5]
	v_cndmask_b32_e64 v21, v21, v199, s[6:7]
	v_cndmask_b32_e64 v22, v22, v199, s[8:9]
	v_cndmask_b32_e64 v23, v23, v199, s[10:11]
	v_cndmask_b32_e64 v24, v24, v199, s[12:13]
	v_cndmask_b32_e64 v25, v25, v199, s[14:15]
	v_cndmask_b32_e64 v26, v26, v199, s[16:17]
	v_cndmask_b32_e64 v27, v27, v199, s[18:19]
	v_cndmask_b32_e64 v28, v28, v199, s[20:21]
	v_cndmask_b32_e64 v29, v29, v199, s[22:23]
	v_cndmask_b32_e64 v30, v30, v199, s[24:25]
	v_cndmask_b32_e64 v31, v31, v199, s[26:27]
	v_cndmask_b32_e64 v32, v32, v199, s[28:29]
	v_cndmask_b32_e64 v33, v33, v199, s[30:31]
.Lq2_nd1_3:
	s_nop 3
	s_waitcnt vmcnt(6)
	v_mfma_scale_f32_32x32x64_f8f6f4 v[2:17], v[34:41], v[106:113], 0, v203, v203 op_sel_hi:[0,0,0]
	ds_read_b128 v[236:239], v202 offset:64
	v_exp_f32_e64 v18, -v18
	v_exp_f32_e64 v19, -v19
	v_exp_f32_e64 v20, -v20
	v_exp_f32_e64 v21, -v21
	v_add_co_u32_e64 v200, s[42:43], v200, v200
	v_add_co_u32_e64 v200, s[48:49], v200, v200
	v_add_co_u32_e64 v200, s[50:51], v200, v200
	v_add_co_u32_e64 v200, s[56:57], v200, v200
	v_add_f32_e32 v18, v18, v178
	v_add_f32_e32 v19, v19, v179
	v_add_f32_e32 v20, v20, v180
	v_add_f32_e32 v21, v21, v181
	v_cndmask_b32_e64 v18, 1.0, v18, s[42:43]
	v_cndmask_b32_e64 v19, 1.0, v19, s[48:49]
	v_cndmask_b32_e64 v20, 1.0, v20, s[50:51]
	v_cndmask_b32_e64 v21, 1.0, v21, s[56:57]
	v_mul_f32_e32 v18, v220, v18
	v_mul_f32_e32 v19, v221, v19
	v_mul_f32_e32 v20, v222, v20
	v_mul_f32_e32 v21, v223, v21
	v_log_f32_e32 v18, v18
	v_log_f32_e32 v19, v19
	v_log_f32_e32 v20, v20
	v_log_f32_e32 v21, v21
	s_waitcnt lgkmcnt(0)
	v_fmac_f32_e32 v201, v18, v236
	v_fmac_f32_e32 v201, v19, v237
	v_fmac_f32_e32 v201, v20, v238
	v_fmac_f32_e32 v201, v21, v239
	s_waitcnt vmcnt(4)
	v_mfma_scale_f32_32x32x64_f8f6f4 v[2:17], v[42:49], v[122:129], v[2:17], v203, v203 op_sel_hi:[0,0,0]
	ds_read_b128 v[236:239], v202 offset:80
	v_exp_f32_e64 v22, -v22
	v_exp_f32_e64 v23, -v23
	v_exp_f32_e64 v24, -v24
	v_exp_f32_e64 v25, -v25
	v_add_co_u32_e64 v200, s[42:43], v200, v200
	v_add_co_u32_e64 v200, s[48:49], v200, v200
	v_add_co_u32_e64 v200, s[50:51], v200, v200
	v_add_co_u32_e64 v200, s[56:57], v200, v200
	v_add_f32_e32 v22, v22, v182
	v_add_f32_e32 v23, v23, v183
	v_add_f32_e32 v24, v24, v184
	v_add_f32_e32 v25, v25, v185
	v_cndmask_b32_e64 v22, 1.0, v22, s[42:43]
	v_cndmask_b32_e64 v23, 1.0, v23, s[48:49]
	v_cndmask_b32_e64 v24, 1.0, v24, s[50:51]
	v_cndmask_b32_e64 v25, 1.0, v25, s[56:57]
	v_mul_f32_e32 v22, v224, v22
	v_mul_f32_e32 v23, v225, v23
	v_mul_f32_e32 v24, v226, v24
	v_mul_f32_e32 v25, v227, v25
	v_log_f32_e32 v22, v22
	v_log_f32_e32 v23, v23
	v_log_f32_e32 v24, v24
	v_log_f32_e32 v25, v25
	s_waitcnt lgkmcnt(0)
	v_fmac_f32_e32 v201, v22, v236
	v_fmac_f32_e32 v201, v23, v237
	v_fmac_f32_e32 v201, v24, v238
	v_fmac_f32_e32 v201, v25, v239
	s_waitcnt vmcnt(2)
	v_mfma_scale_f32_32x32x64_f8f6f4 v[2:17], v[50:57], v[114:121], v[2:17], v203, v203 op_sel_hi:[0,0,0]
	ds_read_b128 v[236:239], v202 offset:96
	v_exp_f32_e64 v26, -v26
	v_exp_f32_e64 v27, -v27
	v_exp_f32_e64 v28, -v28
	v_exp_f32_e64 v29, -v29
	v_add_co_u32_e64 v200, s[42:43], v200, v200
	v_add_co_u32_e64 v200, s[48:49], v200, v200
	v_add_co_u32_e64 v200, s[50:51], v200, v200
	v_add_co_u32_e64 v200, s[56:57], v200, v200
	v_add_f32_e32 v26, v26, v186
	v_add_f32_e32 v27, v27, v187
	v_add_f32_e32 v28, v28, v188
	v_add_f32_e32 v29, v29, v189
	v_cndmask_b32_e64 v26, 1.0, v26, s[42:43]
	v_cndmask_b32_e64 v27, 1.0, v27, s[48:49]
	v_cndmask_b32_e64 v28, 1.0, v28, s[50:51]
	v_cndmask_b32_e64 v29, 1.0, v29, s[56:57]
	v_mul_f32_e32 v26, v228, v26
	v_mul_f32_e32 v27, v229, v27
	v_mul_f32_e32 v28, v230, v28
	v_mul_f32_e32 v29, v231, v29
	v_log_f32_e32 v26, v26
	v_log_f32_e32 v27, v27
	v_log_f32_e32 v28, v28
	v_log_f32_e32 v29, v29
	s_waitcnt lgkmcnt(0)
	v_fmac_f32_e32 v201, v26, v236
	v_fmac_f32_e32 v201, v27, v237
	v_fmac_f32_e32 v201, v28, v238
	v_fmac_f32_e32 v201, v29, v239
	s_waitcnt vmcnt(0)
	v_mfma_scale_f32_32x32x64_f8f6f4 v[2:17], v[58:65], v[98:105], v[2:17], v203, v203 op_sel_hi:[0,0,0]
	ds_read_b128 v[236:239], v202 offset:112
	v_exp_f32_e64 v30, -v30
	v_exp_f32_e64 v31, -v31
	v_exp_f32_e64 v32, -v32
	v_exp_f32_e64 v33, -v33
	v_add_co_u32_e64 v200, s[42:43], v200, v200
	v_add_co_u32_e64 v200, s[48:49], v200, v200
	v_add_co_u32_e64 v200, s[50:51], v200, v200
	v_add_co_u32_e64 v200, s[56:57], v200, v200
	v_add_f32_e32 v30, v30, v190
	v_add_f32_e32 v31, v31, v191
	v_add_f32_e32 v32, v32, v192
	v_add_f32_e32 v33, v33, v193
	v_cndmask_b32_e64 v30, 1.0, v30, s[42:43]
	v_cndmask_b32_e64 v31, 1.0, v31, s[48:49]
	v_cndmask_b32_e64 v32, 1.0, v32, s[50:51]
	v_cndmask_b32_e64 v33, 1.0, v33, s[56:57]
	v_mul_f32_e32 v30, v232, v30
	v_mul_f32_e32 v31, v233, v31
	v_mul_f32_e32 v32, v234, v32
	v_mul_f32_e32 v33, v235, v33
	v_log_f32_e32 v30, v30
	v_log_f32_e32 v31, v31
	v_log_f32_e32 v32, v32
	v_log_f32_e32 v33, v33
	s_waitcnt lgkmcnt(0)
	v_fmac_f32_e32 v201, v30, v236
	v_fmac_f32_e32 v201, v31, v237
	v_fmac_f32_e32 v201, v32, v238
	v_fmac_f32_e32 v201, v33, v239
	s_add_i32 s39, s39, 1
	s_cmp_lt_u32 s39, 4
	s_cbranch_scc1 .Lq2_loop

.LBB1_105:
	s_or_b64 exec, exec, s[2:3]
	s_andn2_b64 vcc, exec, s[36:37]
	s_waitcnt lgkmcnt(0)
	s_barrier
	s_cbranch_vccnz .LBB1_111
	v_lshl_or_b32 v8, v196, 7, v197
	ds_read_b32 v8, v8 offset:36864
	s_waitcnt lgkmcnt(0)
	v_cmp_lt_f32_e32 vcc, 0, v8
	v_lshl_or_b32 v9, v196, 7, v197
	ds_read_b32 v9, v9 offset:37376
	s_waitcnt lgkmcnt(0)
	v_log_f32_e32 v9, v9
	s_nop 1
	v_cndmask_b32_e32 v9, 0, v9, vcc
	s_nop 1
	v_add_f32_dpp v9, v9, v9 quad_perm:[1,0,3,2] row_mask:0xf bank_mask:0xf bound_ctrl:1
	s_nop 1
	v_add_f32_dpp v9, v9, v9 quad_perm:[2,3,0,1] row_mask:0xf bank_mask:0xf bound_ctrl:1
	s_nop 1
	v_add_f32_dpp v9, v9, v9 row_half_mirror row_mask:0xf bank_mask:0xf bound_ctrl:1
	s_nop 1
	v_add_f32_dpp v9, v9, v9 row_mirror row_mask:0xf bank_mask:0xf bound_ctrl:1
	s_nop 1
	v_add_f32_dpp v9, v9, v9 row_bcast:15 row_mask:0xa bank_mask:0xf bound_ctrl:1
	s_nop 1
	v_add_f32_dpp v9, v9, v9 row_bcast:31 row_mask:0xc bank_mask:0xf bound_ctrl:1
	s_nop 1
	v_readlane_b32 s16, v9, 63
	s_nop 3
	s_and_saveexec_b64 s[2:3], s[0:1]
	s_cbranch_execz .LBB1_110
	v_mov_b32_e32 v8, 0
	ds_read_b128 v[10:13], v8 offset:37632
	ds_read_b128 v[14:17], v8 offset:37648
	v_readlane_b32 s6, v240, 0
	v_readlane_b32 s7, v240, 1
	v_readlane_b32 s8, v240, 6
	s_ashr_i32 s7, s6, 31
	v_readlane_b32 s10, v240, 8
	v_readlane_b32 s11, v240, 9
	v_readlane_b32 s14, v240, 12
	v_readlane_b32 s15, v240, 13
	s_lshl_b64 s[6:7], s[6:7], 2
	s_mov_b64 s[10:11], s[14:15]
	s_waitcnt lgkmcnt(1)
	v_add_f32_e32 v9, 0, v10
	s_add_u32 s6, s10, s6
	s_flbit_i32_b32 s8, 0
	s_mov_b32 s5, 0
	v_add_f32_e32 v9, v9, v11
	s_addc_u32 s7, s11, s7
	s_bcnt1_i32_b64 s4, vcc
	s_min_u32 s8, s8, 32
	v_add_f32_e32 v9, v9, v12
	s_lshl_b64 s[4:5], s[4:5], s8
	v_add_f32_e32 v9, v9, v13
	s_min_u32 s4, s4, 1
	s_waitcnt lgkmcnt(0)
	v_add_f32_e32 v9, v9, v14
	s_or_b32 s4, s5, s4
	v_add_f32_e32 v9, v9, v15
	v_cvt_f32_u32_e32 v10, s4
	v_add_f32_e32 v9, v9, v16
	v_add_f32_e32 v9, v9, v17
	v_subrev_f32_e32 v9, s16, v9
	v_mul_f32_e32 v9, 0x3f317218, v9
	s_sub_i32 s4, 32, s8
	s_mov_b64 s[0:1], exec
	global_store_dword v8, v9, s[6:7] sc1
	v_ldexp_f32 v9, v10, s4
	global_store_dword v8, v9, s[6:7] offset:4 sc1
	v_mbcnt_lo_u32_b32 v9, s0, 0
	v_mbcnt_hi_u32_b32 v9, s1, v9
	v_cmp_eq_u32_e32 vcc, 0, v9
	v_readlane_b32 s9, v240, 7
	v_readlane_b32 s12, v240, 10
	v_readlane_b32 s13, v240, 11
	s_and_saveexec_b64 s[4:5], vcc
	s_cbranch_execz .LBB1_109
	s_bcnt1_i32_b64 s0, s[0:1]
	v_readlane_b32 s8, v240, 2
	v_mov_b32_e32 v10, s0
	v_readlane_b32 s9, v240, 3
	v_readlane_b32 s10, v240, 4
	v_readlane_b32 s11, v240, 5
	s_waitcnt vmcnt(0)
	s_nop 0
	global_atomic_add v10, v8, v10, s[8:9] sc0
	s_waitcnt vmcnt(0)
